# P7 fixed conversion share: 2x4 concurrent window plus a per-workgroup start phase of the column sweep (workgroups no longer sweep the same columns in lockstep)
# speedup vs baseline: 1.0001x; 1.0001x over previous
.LBB0_993:
	s_add_u32 s38, s90, 0x4b100000
	s_addc_u32 s39, s91, 0
	v_readlane_b32 s3, v255, 4
	s_bitcmp0_b32 s3, 0
	s_cbranch_scc1 .LBB0_1024
	s_waitcnt vmcnt(0)
	v_readlane_b32 s2, v255, 28
	s_lshl_b32 s0, s3, 6
	s_and_b32 s0, s0, 0xffffff80
	s_and_b32 s1, s2, 1
	s_lshl_b32 s1, s1, 6
	s_lshr_b32 s2, s2, 1
	s_add_i32 s2, s2, s1
	s_add_i32 s20, s2, s0
	s_lshr_b32 s21, s3, 1
	s_and_b32 s21, s21, 15
	v_mbcnt_lo_u32_b32 v210, -1, 0
	v_mbcnt_hi_u32_b32 v210, -1, v210
	v_lshrrev_b32_e32 v211, 3, v210
	v_and_b32_e32 v210, 7, v210
	v_lshlrev_b32_e32 v208, 17, v211
	v_lshl_or_b32 v208, v210, 4, v208
	v_lshlrev_b32_e32 v209, 13, v210
	v_lshl_or_b32 v209, v211, 4, v209
	s_mov_b32 s16, 0x44000000
	s_add_i32 s1, s21, 0
	s_and_b32 s1, s1, 15
	s_lshl_b32 s1, s1, 2
	s_add_i32 s1, s1, s20
	s_lshr_b32 s2, s1, 10
	s_and_b32 s4, s1, 0x3ff
	s_lshr_b32 s5, s4, 6
	s_and_b32 s4, s4, 63
	s_lshl_b32 s12, s2, 24
	s_lshl_b32 s13, s5, 20
	s_add_i32 s12, s12, s13
	s_lshl_b32 s13, s4, 7
	s_add_i32 s12, s12, s13
	s_add_u32 s14, s70, s12
	s_addc_u32 s15, s71, 0
	global_load_dwordx4 v[0:3], v208, s[14:15] sc1 nt
	s_add_u32 s18, s14, 0x2000
	s_addc_u32 s19, s15, 0
	global_load_dwordx4 v[4:7], v208, s[18:19] sc1 nt
	s_add_u32 s18, s14, 0x4000
	s_addc_u32 s19, s15, 0
	global_load_dwordx4 v[8:11], v208, s[18:19] sc1 nt
	s_add_u32 s18, s14, 0x6000
	s_addc_u32 s19, s15, 0
	global_load_dwordx4 v[12:15], v208, s[18:19] sc1 nt
	s_add_u32 s18, s14, 0x8000
	s_addc_u32 s19, s15, 0
	global_load_dwordx4 v[16:19], v208, s[18:19] sc1 nt
	s_add_u32 s18, s14, 0xa000
	s_addc_u32 s19, s15, 0
	global_load_dwordx4 v[20:23], v208, s[18:19] sc1 nt
	s_add_u32 s18, s14, 0xc000
	s_addc_u32 s19, s15, 0
	global_load_dwordx4 v[24:27], v208, s[18:19] sc1 nt
	s_add_u32 s18, s14, 0xe000
	s_addc_u32 s19, s15, 0
	global_load_dwordx4 v[28:31], v208, s[18:19] sc1 nt
	s_add_u32 s18, s14, 0x10000
	s_addc_u32 s19, s15, 0
	global_load_dwordx4 v[32:35], v208, s[18:19] sc1 nt
	s_add_u32 s18, s14, 0x12000
	s_addc_u32 s19, s15, 0
	global_load_dwordx4 v[36:39], v208, s[18:19] sc1 nt
	s_add_u32 s18, s14, 0x14000
	s_addc_u32 s19, s15, 0
	global_load_dwordx4 v[40:43], v208, s[18:19] sc1 nt
	s_add_u32 s18, s14, 0x16000
	s_addc_u32 s19, s15, 0
	global_load_dwordx4 v[44:47], v208, s[18:19] sc1 nt
	s_add_u32 s18, s14, 0x18000
	s_addc_u32 s19, s15, 0
	global_load_dwordx4 v[48:51], v208, s[18:19] sc1 nt
	s_add_u32 s18, s14, 0x1a000
	s_addc_u32 s19, s15, 0
	global_load_dwordx4 v[52:55], v208, s[18:19] sc1 nt
	s_add_u32 s18, s14, 0x1c000
	s_addc_u32 s19, s15, 0
	global_load_dwordx4 v[56:59], v208, s[18:19] sc1 nt
	s_add_u32 s18, s14, 0x1e000
	s_addc_u32 s19, s15, 0
	global_load_dwordx4 v[60:63], v208, s[18:19] sc1 nt
	s_add_i32 s1, s21, 1
	s_and_b32 s1, s1, 15
	s_lshl_b32 s1, s1, 2
	s_add_i32 s1, s1, s20
	s_lshr_b32 s2, s1, 10
	s_and_b32 s4, s1, 0x3ff
	s_lshr_b32 s5, s4, 6
	s_and_b32 s4, s4, 63
	s_lshl_b32 s12, s2, 24
	s_lshl_b32 s13, s5, 20
	s_add_i32 s12, s12, s13
	s_lshl_b32 s13, s4, 7
	s_add_i32 s12, s12, s13
	s_add_u32 s14, s70, s12
	s_addc_u32 s15, s71, 0
	global_load_dwordx4 v[64:67], v208, s[14:15] sc1 nt
	s_add_u32 s18, s14, 0x2000
	s_addc_u32 s19, s15, 0
	global_load_dwordx4 v[68:71], v208, s[18:19] sc1 nt
	s_add_u32 s18, s14, 0x4000
	s_addc_u32 s19, s15, 0
	global_load_dwordx4 v[72:75], v208, s[18:19] sc1 nt
	s_add_u32 s18, s14, 0x6000
	s_addc_u32 s19, s15, 0
	global_load_dwordx4 v[76:79], v208, s[18:19] sc1 nt
	s_add_u32 s18, s14, 0x8000
	s_addc_u32 s19, s15, 0
	global_load_dwordx4 v[80:83], v208, s[18:19] sc1 nt
	s_add_u32 s18, s14, 0xa000
	s_addc_u32 s19, s15, 0
	global_load_dwordx4 v[84:87], v208, s[18:19] sc1 nt
	s_add_u32 s18, s14, 0xc000
	s_addc_u32 s19, s15, 0
	global_load_dwordx4 v[88:91], v208, s[18:19] sc1 nt
	s_add_u32 s18, s14, 0xe000
	s_addc_u32 s19, s15, 0
	global_load_dwordx4 v[92:95], v208, s[18:19] sc1 nt
	s_add_u32 s18, s14, 0x10000
	s_addc_u32 s19, s15, 0
	global_load_dwordx4 v[96:99], v208, s[18:19] sc1 nt
	s_add_u32 s18, s14, 0x12000
	s_addc_u32 s19, s15, 0
	global_load_dwordx4 v[100:103], v208, s[18:19] sc1 nt
	s_add_u32 s18, s14, 0x14000
	s_addc_u32 s19, s15, 0
	global_load_dwordx4 v[104:107], v208, s[18:19] sc1 nt
	s_add_u32 s18, s14, 0x16000
	s_addc_u32 s19, s15, 0
	global_load_dwordx4 v[108:111], v208, s[18:19] sc1 nt
	s_add_u32 s18, s14, 0x18000
	s_addc_u32 s19, s15, 0
	global_load_dwordx4 v[112:115], v208, s[18:19] sc1 nt
	s_add_u32 s18, s14, 0x1a000
	s_addc_u32 s19, s15, 0
	global_load_dwordx4 v[116:119], v208, s[18:19] sc1 nt
	s_add_u32 s18, s14, 0x1c000
	s_addc_u32 s19, s15, 0
	global_load_dwordx4 v[120:123], v208, s[18:19] sc1 nt
	s_add_u32 s18, s14, 0x1e000
	s_addc_u32 s19, s15, 0
	global_load_dwordx4 v[124:127], v208, s[18:19] sc1 nt
	s_add_i32 s1, s21, 2
	s_and_b32 s1, s1, 15
	s_lshl_b32 s1, s1, 2
	s_add_i32 s1, s1, s20
	s_lshr_b32 s2, s1, 10
	s_and_b32 s4, s1, 0x3ff
	s_lshr_b32 s5, s4, 6
	s_and_b32 s4, s4, 63
	s_lshl_b32 s12, s2, 24
	s_lshl_b32 s13, s5, 20
	s_add_i32 s12, s12, s13
	s_lshl_b32 s13, s4, 7
	s_add_i32 s12, s12, s13
	s_add_u32 s14, s70, s12
	s_addc_u32 s15, s71, 0
	global_load_dwordx4 v[128:131], v208, s[14:15] sc1 nt
	s_add_u32 s18, s14, 0x2000
	s_addc_u32 s19, s15, 0
	global_load_dwordx4 v[132:135], v208, s[18:19] sc1 nt
	s_add_u32 s18, s14, 0x4000
	s_addc_u32 s19, s15, 0
	global_load_dwordx4 v[136:139], v208, s[18:19] sc1 nt
	s_add_u32 s18, s14, 0x6000
	s_addc_u32 s19, s15, 0
	global_load_dwordx4 v[140:143], v208, s[18:19] sc1 nt
	s_add_u32 s18, s14, 0x8000
	s_addc_u32 s19, s15, 0
	global_load_dwordx4 v[144:147], v208, s[18:19] sc1 nt
	s_add_u32 s18, s14, 0xa000
	s_addc_u32 s19, s15, 0
	global_load_dwordx4 v[148:151], v208, s[18:19] sc1 nt
	s_add_u32 s18, s14, 0xc000
	s_addc_u32 s19, s15, 0
	global_load_dwordx4 v[152:155], v208, s[18:19] sc1 nt
	s_add_u32 s18, s14, 0xe000
	s_addc_u32 s19, s15, 0
	global_load_dwordx4 v[156:159], v208, s[18:19] sc1 nt
	s_add_u32 s18, s14, 0x10000
	s_addc_u32 s19, s15, 0
	global_load_dwordx4 v[160:163], v208, s[18:19] sc1 nt
	s_add_u32 s18, s14, 0x12000
	s_addc_u32 s19, s15, 0
	global_load_dwordx4 v[164:167], v208, s[18:19] sc1 nt
	s_add_u32 s18, s14, 0x14000
	s_addc_u32 s19, s15, 0
	global_load_dwordx4 v[168:171], v208, s[18:19] sc1 nt
	s_add_u32 s18, s14, 0x16000
	s_addc_u32 s19, s15, 0
	global_load_dwordx4 v[172:175], v208, s[18:19] sc1 nt
	s_add_u32 s18, s14, 0x18000
	s_addc_u32 s19, s15, 0
	global_load_dwordx4 v[176:179], v208, s[18:19] sc1 nt
	s_add_u32 s18, s14, 0x1a000
	s_addc_u32 s19, s15, 0
	global_load_dwordx4 v[180:183], v208, s[18:19] sc1 nt
	s_add_u32 s18, s14, 0x1c000
	s_addc_u32 s19, s15, 0
	global_load_dwordx4 v[184:187], v208, s[18:19] sc1 nt
	s_add_u32 s18, s14, 0x1e000
	s_addc_u32 s19, s15, 0
	global_load_dwordx4 v[188:191], v208, s[18:19] sc1 nt
	s_waitcnt vmcnt(32)
	s_add_i32 s1, s21, 0
	s_and_b32 s1, s1, 15
	s_lshl_b32 s1, s1, 2
	s_add_i32 s1, s1, s20
	s_lshr_b32 s2, s1, 10
	s_and_b32 s4, s1, 0x3ff
	s_lshr_b32 s5, s4, 6
	s_and_b32 s4, s4, 63
	s_lshl_b32 s12, s2, 22
	s_lshl_b32 s13, s4, 16
	s_add_i32 s12, s12, s13
	s_lshl_b32 s13, s5, 7
	s_add_i32 s12, s12, s13
	s_add_u32 s24, s90, s12
	s_addc_u32 s25, s91, 0
	s_add_u32 s24, s24, 0x3b100000
	s_addc_u32 s25, s25, 0
	s_add_u32 s26, s24, 0x1000
	s_addc_u32 s27, s25, 0
	v_pk_mul_f32 v[0:1], v[0:1], s[16:17] op_sel_hi:[1,0]
	v_pk_mul_f32 v[2:3], v[2:3], s[16:17] op_sel_hi:[1,0]
	v_pk_mul_f32 v[4:5], v[4:5], s[16:17] op_sel_hi:[1,0]
	v_pk_mul_f32 v[6:7], v[6:7], s[16:17] op_sel_hi:[1,0]
	v_pk_mul_f32 v[8:9], v[8:9], s[16:17] op_sel_hi:[1,0]
	v_pk_mul_f32 v[10:11], v[10:11], s[16:17] op_sel_hi:[1,0]
	v_pk_mul_f32 v[12:13], v[12:13], s[16:17] op_sel_hi:[1,0]
	v_pk_mul_f32 v[14:15], v[14:15], s[16:17] op_sel_hi:[1,0]
	v_pk_mul_f32 v[16:17], v[16:17], s[16:17] op_sel_hi:[1,0]
	v_pk_mul_f32 v[18:19], v[18:19], s[16:17] op_sel_hi:[1,0]
	v_pk_mul_f32 v[20:21], v[20:21], s[16:17] op_sel_hi:[1,0]
	v_pk_mul_f32 v[22:23], v[22:23], s[16:17] op_sel_hi:[1,0]
	v_pk_mul_f32 v[24:25], v[24:25], s[16:17] op_sel_hi:[1,0]
	v_pk_mul_f32 v[26:27], v[26:27], s[16:17] op_sel_hi:[1,0]
	v_pk_mul_f32 v[28:29], v[28:29], s[16:17] op_sel_hi:[1,0]
	v_pk_mul_f32 v[30:31], v[30:31], s[16:17] op_sel_hi:[1,0]
	v_pk_mul_f32 v[32:33], v[32:33], s[16:17] op_sel_hi:[1,0]
	v_pk_mul_f32 v[34:35], v[34:35], s[16:17] op_sel_hi:[1,0]
	v_pk_mul_f32 v[36:37], v[36:37], s[16:17] op_sel_hi:[1,0]
	v_pk_mul_f32 v[38:39], v[38:39], s[16:17] op_sel_hi:[1,0]
	v_pk_mul_f32 v[40:41], v[40:41], s[16:17] op_sel_hi:[1,0]
	v_pk_mul_f32 v[42:43], v[42:43], s[16:17] op_sel_hi:[1,0]
	v_pk_mul_f32 v[44:45], v[44:45], s[16:17] op_sel_hi:[1,0]
	v_pk_mul_f32 v[46:47], v[46:47], s[16:17] op_sel_hi:[1,0]
	v_pk_mul_f32 v[48:49], v[48:49], s[16:17] op_sel_hi:[1,0]
	v_pk_mul_f32 v[50:51], v[50:51], s[16:17] op_sel_hi:[1,0]
	v_pk_mul_f32 v[52:53], v[52:53], s[16:17] op_sel_hi:[1,0]
	v_pk_mul_f32 v[54:55], v[54:55], s[16:17] op_sel_hi:[1,0]
	v_pk_mul_f32 v[56:57], v[56:57], s[16:17] op_sel_hi:[1,0]
	v_pk_mul_f32 v[58:59], v[58:59], s[16:17] op_sel_hi:[1,0]
	v_pk_mul_f32 v[60:61], v[60:61], s[16:17] op_sel_hi:[1,0]
	v_pk_mul_f32 v[62:63], v[62:63], s[16:17] op_sel_hi:[1,0]
	v_cvt_pk_fp8_f32 v192, v0, v4
	v_cvt_pk_fp8_f32 v192, v8, v12 op_sel:[0,0,1]
	v_cvt_pk_fp8_f32 v193, v16, v20
	v_cvt_pk_fp8_f32 v193, v24, v28 op_sel:[0,0,1]
	v_cvt_pk_fp8_f32 v194, v32, v36
	v_cvt_pk_fp8_f32 v194, v40, v44 op_sel:[0,0,1]
	v_cvt_pk_fp8_f32 v195, v48, v52
	v_cvt_pk_fp8_f32 v195, v56, v60 op_sel:[0,0,1]
	global_store_dwordx4 v209, v[192:195], s[24:25] sc1
	v_cvt_pk_fp8_f32 v196, v1, v5
	v_cvt_pk_fp8_f32 v196, v9, v13 op_sel:[0,0,1]
	v_cvt_pk_fp8_f32 v197, v17, v21
	v_cvt_pk_fp8_f32 v197, v25, v29 op_sel:[0,0,1]
	v_cvt_pk_fp8_f32 v198, v33, v37
	v_cvt_pk_fp8_f32 v198, v41, v45 op_sel:[0,0,1]
	v_cvt_pk_fp8_f32 v199, v49, v53
	v_cvt_pk_fp8_f32 v199, v57, v61 op_sel:[0,0,1]
	global_store_dwordx4 v209, v[196:199], s[24:25] offset:2048 sc1
	v_cvt_pk_fp8_f32 v200, v2, v6
	v_cvt_pk_fp8_f32 v200, v10, v14 op_sel:[0,0,1]
	v_cvt_pk_fp8_f32 v201, v18, v22
	v_cvt_pk_fp8_f32 v201, v26, v30 op_sel:[0,0,1]
	v_cvt_pk_fp8_f32 v202, v34, v38
	v_cvt_pk_fp8_f32 v202, v42, v46 op_sel:[0,0,1]
	v_cvt_pk_fp8_f32 v203, v50, v54
	v_cvt_pk_fp8_f32 v203, v58, v62 op_sel:[0,0,1]
	global_store_dwordx4 v209, v[200:203], s[26:27] sc1
	v_cvt_pk_fp8_f32 v204, v3, v7
	v_cvt_pk_fp8_f32 v204, v11, v15 op_sel:[0,0,1]
	v_cvt_pk_fp8_f32 v205, v19, v23
	v_cvt_pk_fp8_f32 v205, v27, v31 op_sel:[0,0,1]
	v_cvt_pk_fp8_f32 v206, v35, v39
	v_cvt_pk_fp8_f32 v206, v43, v47 op_sel:[0,0,1]
	v_cvt_pk_fp8_f32 v207, v51, v55
	v_cvt_pk_fp8_f32 v207, v59, v63 op_sel:[0,0,1]
	global_store_dwordx4 v209, v[204:207], s[26:27] offset:2048 sc1
	s_add_i32 s1, s21, 3
	s_and_b32 s1, s1, 15
	s_lshl_b32 s1, s1, 2
	s_add_i32 s1, s1, s20
	s_lshr_b32 s2, s1, 10
	s_and_b32 s4, s1, 0x3ff
	s_lshr_b32 s5, s4, 6
	s_and_b32 s4, s4, 63
	s_lshl_b32 s12, s2, 24
	s_lshl_b32 s13, s5, 20
	s_add_i32 s12, s12, s13
	s_lshl_b32 s13, s4, 7
	s_add_i32 s12, s12, s13
	s_add_u32 s14, s70, s12
	s_addc_u32 s15, s71, 0
	global_load_dwordx4 v[0:3], v208, s[14:15] sc1 nt
	s_add_u32 s18, s14, 0x2000
	s_addc_u32 s19, s15, 0
	global_load_dwordx4 v[4:7], v208, s[18:19] sc1 nt
	s_add_u32 s18, s14, 0x4000
	s_addc_u32 s19, s15, 0
	global_load_dwordx4 v[8:11], v208, s[18:19] sc1 nt
	s_add_u32 s18, s14, 0x6000
	s_addc_u32 s19, s15, 0
	global_load_dwordx4 v[12:15], v208, s[18:19] sc1 nt
	s_add_u32 s18, s14, 0x8000
	s_addc_u32 s19, s15, 0
	global_load_dwordx4 v[16:19], v208, s[18:19] sc1 nt
	s_add_u32 s18, s14, 0xa000
	s_addc_u32 s19, s15, 0
	global_load_dwordx4 v[20:23], v208, s[18:19] sc1 nt
	s_add_u32 s18, s14, 0xc000
	s_addc_u32 s19, s15, 0
	global_load_dwordx4 v[24:27], v208, s[18:19] sc1 nt
	s_add_u32 s18, s14, 0xe000
	s_addc_u32 s19, s15, 0
	global_load_dwordx4 v[28:31], v208, s[18:19] sc1 nt
	s_add_u32 s18, s14, 0x10000
	s_addc_u32 s19, s15, 0
	global_load_dwordx4 v[32:35], v208, s[18:19] sc1 nt
	s_add_u32 s18, s14, 0x12000
	s_addc_u32 s19, s15, 0
	global_load_dwordx4 v[36:39], v208, s[18:19] sc1 nt
	s_add_u32 s18, s14, 0x14000
	s_addc_u32 s19, s15, 0
	global_load_dwordx4 v[40:43], v208, s[18:19] sc1 nt
	s_add_u32 s18, s14, 0x16000
	s_addc_u32 s19, s15, 0
	global_load_dwordx4 v[44:47], v208, s[18:19] sc1 nt
	s_add_u32 s18, s14, 0x18000
	s_addc_u32 s19, s15, 0
	global_load_dwordx4 v[48:51], v208, s[18:19] sc1 nt
	s_add_u32 s18, s14, 0x1a000
	s_addc_u32 s19, s15, 0
	global_load_dwordx4 v[52:55], v208, s[18:19] sc1 nt
	s_add_u32 s18, s14, 0x1c000
	s_addc_u32 s19, s15, 0
	global_load_dwordx4 v[56:59], v208, s[18:19] sc1 nt
	s_add_u32 s18, s14, 0x1e000
	s_addc_u32 s19, s15, 0
	global_load_dwordx4 v[60:63], v208, s[18:19] sc1 nt
	s_waitcnt vmcnt(36)
	s_add_i32 s1, s21, 1
	s_and_b32 s1, s1, 15
	s_lshl_b32 s1, s1, 2
	s_add_i32 s1, s1, s20
	s_lshr_b32 s2, s1, 10
	s_and_b32 s4, s1, 0x3ff
	s_lshr_b32 s5, s4, 6
	s_and_b32 s4, s4, 63
	s_lshl_b32 s12, s2, 22
	s_lshl_b32 s13, s4, 16
	s_add_i32 s12, s12, s13
	s_lshl_b32 s13, s5, 7
	s_add_i32 s12, s12, s13
	s_add_u32 s24, s90, s12
	s_addc_u32 s25, s91, 0
	s_add_u32 s24, s24, 0x3b100000
	s_addc_u32 s25, s25, 0
	s_add_u32 s26, s24, 0x1000
	s_addc_u32 s27, s25, 0
	v_pk_mul_f32 v[64:65], v[64:65], s[16:17] op_sel_hi:[1,0]
	v_pk_mul_f32 v[66:67], v[66:67], s[16:17] op_sel_hi:[1,0]
	v_pk_mul_f32 v[68:69], v[68:69], s[16:17] op_sel_hi:[1,0]
	v_pk_mul_f32 v[70:71], v[70:71], s[16:17] op_sel_hi:[1,0]
	v_pk_mul_f32 v[72:73], v[72:73], s[16:17] op_sel_hi:[1,0]
	v_pk_mul_f32 v[74:75], v[74:75], s[16:17] op_sel_hi:[1,0]
	v_pk_mul_f32 v[76:77], v[76:77], s[16:17] op_sel_hi:[1,0]
	v_pk_mul_f32 v[78:79], v[78:79], s[16:17] op_sel_hi:[1,0]
	v_pk_mul_f32 v[80:81], v[80:81], s[16:17] op_sel_hi:[1,0]
	v_pk_mul_f32 v[82:83], v[82:83], s[16:17] op_sel_hi:[1,0]
	v_pk_mul_f32 v[84:85], v[84:85], s[16:17] op_sel_hi:[1,0]
	v_pk_mul_f32 v[86:87], v[86:87], s[16:17] op_sel_hi:[1,0]
	v_pk_mul_f32 v[88:89], v[88:89], s[16:17] op_sel_hi:[1,0]
	v_pk_mul_f32 v[90:91], v[90:91], s[16:17] op_sel_hi:[1,0]
	v_pk_mul_f32 v[92:93], v[92:93], s[16:17] op_sel_hi:[1,0]
	v_pk_mul_f32 v[94:95], v[94:95], s[16:17] op_sel_hi:[1,0]
	v_pk_mul_f32 v[96:97], v[96:97], s[16:17] op_sel_hi:[1,0]
	v_pk_mul_f32 v[98:99], v[98:99], s[16:17] op_sel_hi:[1,0]
	v_pk_mul_f32 v[100:101], v[100:101], s[16:17] op_sel_hi:[1,0]
	v_pk_mul_f32 v[102:103], v[102:103], s[16:17] op_sel_hi:[1,0]
	v_pk_mul_f32 v[104:105], v[104:105], s[16:17] op_sel_hi:[1,0]
	v_pk_mul_f32 v[106:107], v[106:107], s[16:17] op_sel_hi:[1,0]
	v_pk_mul_f32 v[108:109], v[108:109], s[16:17] op_sel_hi:[1,0]
	v_pk_mul_f32 v[110:111], v[110:111], s[16:17] op_sel_hi:[1,0]
	v_pk_mul_f32 v[112:113], v[112:113], s[16:17] op_sel_hi:[1,0]
	v_pk_mul_f32 v[114:115], v[114:115], s[16:17] op_sel_hi:[1,0]
	v_pk_mul_f32 v[116:117], v[116:117], s[16:17] op_sel_hi:[1,0]
	v_pk_mul_f32 v[118:119], v[118:119], s[16:17] op_sel_hi:[1,0]
	v_pk_mul_f32 v[120:121], v[120:121], s[16:17] op_sel_hi:[1,0]
	v_pk_mul_f32 v[122:123], v[122:123], s[16:17] op_sel_hi:[1,0]
	v_pk_mul_f32 v[124:125], v[124:125], s[16:17] op_sel_hi:[1,0]
	v_pk_mul_f32 v[126:127], v[126:127], s[16:17] op_sel_hi:[1,0]
	v_cvt_pk_fp8_f32 v192, v64, v68
	v_cvt_pk_fp8_f32 v192, v72, v76 op_sel:[0,0,1]
	v_cvt_pk_fp8_f32 v193, v80, v84
	v_cvt_pk_fp8_f32 v193, v88, v92 op_sel:[0,0,1]
	v_cvt_pk_fp8_f32 v194, v96, v100
	v_cvt_pk_fp8_f32 v194, v104, v108 op_sel:[0,0,1]
	v_cvt_pk_fp8_f32 v195, v112, v116
	v_cvt_pk_fp8_f32 v195, v120, v124 op_sel:[0,0,1]
	global_store_dwordx4 v209, v[192:195], s[24:25] sc1
	v_cvt_pk_fp8_f32 v196, v65, v69
	v_cvt_pk_fp8_f32 v196, v73, v77 op_sel:[0,0,1]
	v_cvt_pk_fp8_f32 v197, v81, v85
	v_cvt_pk_fp8_f32 v197, v89, v93 op_sel:[0,0,1]
	v_cvt_pk_fp8_f32 v198, v97, v101
	v_cvt_pk_fp8_f32 v198, v105, v109 op_sel:[0,0,1]
	v_cvt_pk_fp8_f32 v199, v113, v117
	v_cvt_pk_fp8_f32 v199, v121, v125 op_sel:[0,0,1]
	global_store_dwordx4 v209, v[196:199], s[24:25] offset:2048 sc1
	v_cvt_pk_fp8_f32 v200, v66, v70
	v_cvt_pk_fp8_f32 v200, v74, v78 op_sel:[0,0,1]
	v_cvt_pk_fp8_f32 v201, v82, v86
	v_cvt_pk_fp8_f32 v201, v90, v94 op_sel:[0,0,1]
	v_cvt_pk_fp8_f32 v202, v98, v102
	v_cvt_pk_fp8_f32 v202, v106, v110 op_sel:[0,0,1]
	v_cvt_pk_fp8_f32 v203, v114, v118
	v_cvt_pk_fp8_f32 v203, v122, v126 op_sel:[0,0,1]
	global_store_dwordx4 v209, v[200:203], s[26:27] sc1
	v_cvt_pk_fp8_f32 v204, v67, v71
	v_cvt_pk_fp8_f32 v204, v75, v79 op_sel:[0,0,1]
	v_cvt_pk_fp8_f32 v205, v83, v87
	v_cvt_pk_fp8_f32 v205, v91, v95 op_sel:[0,0,1]
	v_cvt_pk_fp8_f32 v206, v99, v103
	v_cvt_pk_fp8_f32 v206, v107, v111 op_sel:[0,0,1]
	v_cvt_pk_fp8_f32 v207, v115, v119
	v_cvt_pk_fp8_f32 v207, v123, v127 op_sel:[0,0,1]
	global_store_dwordx4 v209, v[204:207], s[26:27] offset:2048 sc1
	s_add_i32 s1, s21, 4
	s_and_b32 s1, s1, 15
	s_lshl_b32 s1, s1, 2
	s_add_i32 s1, s1, s20
	s_lshr_b32 s2, s1, 10
	s_and_b32 s4, s1, 0x3ff
	s_lshr_b32 s5, s4, 6
	s_and_b32 s4, s4, 63
	s_lshl_b32 s12, s2, 24
	s_lshl_b32 s13, s5, 20
	s_add_i32 s12, s12, s13
	s_lshl_b32 s13, s4, 7
	s_add_i32 s12, s12, s13
	s_add_u32 s14, s70, s12
	s_addc_u32 s15, s71, 0
	global_load_dwordx4 v[64:67], v208, s[14:15] sc1 nt
	s_add_u32 s18, s14, 0x2000
	s_addc_u32 s19, s15, 0
	global_load_dwordx4 v[68:71], v208, s[18:19] sc1 nt
	s_add_u32 s18, s14, 0x4000
	s_addc_u32 s19, s15, 0
	global_load_dwordx4 v[72:75], v208, s[18:19] sc1 nt
	s_add_u32 s18, s14, 0x6000
	s_addc_u32 s19, s15, 0
	global_load_dwordx4 v[76:79], v208, s[18:19] sc1 nt
	s_add_u32 s18, s14, 0x8000
	s_addc_u32 s19, s15, 0
	global_load_dwordx4 v[80:83], v208, s[18:19] sc1 nt
	s_add_u32 s18, s14, 0xa000
	s_addc_u32 s19, s15, 0
	global_load_dwordx4 v[84:87], v208, s[18:19] sc1 nt
	s_add_u32 s18, s14, 0xc000
	s_addc_u32 s19, s15, 0
	global_load_dwordx4 v[88:91], v208, s[18:19] sc1 nt
	s_add_u32 s18, s14, 0xe000
	s_addc_u32 s19, s15, 0
	global_load_dwordx4 v[92:95], v208, s[18:19] sc1 nt
	s_add_u32 s18, s14, 0x10000
	s_addc_u32 s19, s15, 0
	global_load_dwordx4 v[96:99], v208, s[18:19] sc1 nt
	s_add_u32 s18, s14, 0x12000
	s_addc_u32 s19, s15, 0
	global_load_dwordx4 v[100:103], v208, s[18:19] sc1 nt
	s_add_u32 s18, s14, 0x14000
	s_addc_u32 s19, s15, 0
	global_load_dwordx4 v[104:107], v208, s[18:19] sc1 nt
	s_add_u32 s18, s14, 0x16000
	s_addc_u32 s19, s15, 0
	global_load_dwordx4 v[108:111], v208, s[18:19] sc1 nt
	s_add_u32 s18, s14, 0x18000
	s_addc_u32 s19, s15, 0
	global_load_dwordx4 v[112:115], v208, s[18:19] sc1 nt
	s_add_u32 s18, s14, 0x1a000
	s_addc_u32 s19, s15, 0
	global_load_dwordx4 v[116:119], v208, s[18:19] sc1 nt
	s_add_u32 s18, s14, 0x1c000
	s_addc_u32 s19, s15, 0
	global_load_dwordx4 v[120:123], v208, s[18:19] sc1 nt
	s_add_u32 s18, s14, 0x1e000
	s_addc_u32 s19, s15, 0
	global_load_dwordx4 v[124:127], v208, s[18:19] sc1 nt
	s_waitcnt vmcnt(40)
	s_add_i32 s1, s21, 2
	s_and_b32 s1, s1, 15
	s_lshl_b32 s1, s1, 2
	s_add_i32 s1, s1, s20
	s_lshr_b32 s2, s1, 10
	s_and_b32 s4, s1, 0x3ff
	s_lshr_b32 s5, s4, 6
	s_and_b32 s4, s4, 63
	s_lshl_b32 s12, s2, 22
	s_lshl_b32 s13, s4, 16
	s_add_i32 s12, s12, s13
	s_lshl_b32 s13, s5, 7
	s_add_i32 s12, s12, s13
	s_add_u32 s24, s90, s12
	s_addc_u32 s25, s91, 0
	s_add_u32 s24, s24, 0x3b100000
	s_addc_u32 s25, s25, 0
	s_add_u32 s26, s24, 0x1000
	s_addc_u32 s27, s25, 0
	v_pk_mul_f32 v[128:129], v[128:129], s[16:17] op_sel_hi:[1,0]
	v_pk_mul_f32 v[130:131], v[130:131], s[16:17] op_sel_hi:[1,0]
	v_pk_mul_f32 v[132:133], v[132:133], s[16:17] op_sel_hi:[1,0]
	v_pk_mul_f32 v[134:135], v[134:135], s[16:17] op_sel_hi:[1,0]
	v_pk_mul_f32 v[136:137], v[136:137], s[16:17] op_sel_hi:[1,0]
	v_pk_mul_f32 v[138:139], v[138:139], s[16:17] op_sel_hi:[1,0]
	v_pk_mul_f32 v[140:141], v[140:141], s[16:17] op_sel_hi:[1,0]
	v_pk_mul_f32 v[142:143], v[142:143], s[16:17] op_sel_hi:[1,0]
	v_pk_mul_f32 v[144:145], v[144:145], s[16:17] op_sel_hi:[1,0]
	v_pk_mul_f32 v[146:147], v[146:147], s[16:17] op_sel_hi:[1,0]
	v_pk_mul_f32 v[148:149], v[148:149], s[16:17] op_sel_hi:[1,0]
	v_pk_mul_f32 v[150:151], v[150:151], s[16:17] op_sel_hi:[1,0]
	v_pk_mul_f32 v[152:153], v[152:153], s[16:17] op_sel_hi:[1,0]
	v_pk_mul_f32 v[154:155], v[154:155], s[16:17] op_sel_hi:[1,0]
	v_pk_mul_f32 v[156:157], v[156:157], s[16:17] op_sel_hi:[1,0]
	v_pk_mul_f32 v[158:159], v[158:159], s[16:17] op_sel_hi:[1,0]
	v_pk_mul_f32 v[160:161], v[160:161], s[16:17] op_sel_hi:[1,0]
	v_pk_mul_f32 v[162:163], v[162:163], s[16:17] op_sel_hi:[1,0]
	v_pk_mul_f32 v[164:165], v[164:165], s[16:17] op_sel_hi:[1,0]
	v_pk_mul_f32 v[166:167], v[166:167], s[16:17] op_sel_hi:[1,0]
	v_pk_mul_f32 v[168:169], v[168:169], s[16:17] op_sel_hi:[1,0]
	v_pk_mul_f32 v[170:171], v[170:171], s[16:17] op_sel_hi:[1,0]
	v_pk_mul_f32 v[172:173], v[172:173], s[16:17] op_sel_hi:[1,0]
	v_pk_mul_f32 v[174:175], v[174:175], s[16:17] op_sel_hi:[1,0]
	v_pk_mul_f32 v[176:177], v[176:177], s[16:17] op_sel_hi:[1,0]
	v_pk_mul_f32 v[178:179], v[178:179], s[16:17] op_sel_hi:[1,0]
	v_pk_mul_f32 v[180:181], v[180:181], s[16:17] op_sel_hi:[1,0]
	v_pk_mul_f32 v[182:183], v[182:183], s[16:17] op_sel_hi:[1,0]
	v_pk_mul_f32 v[184:185], v[184:185], s[16:17] op_sel_hi:[1,0]
	v_pk_mul_f32 v[186:187], v[186:187], s[16:17] op_sel_hi:[1,0]
	v_pk_mul_f32 v[188:189], v[188:189], s[16:17] op_sel_hi:[1,0]
	v_pk_mul_f32 v[190:191], v[190:191], s[16:17] op_sel_hi:[1,0]
	v_cvt_pk_fp8_f32 v192, v128, v132
	v_cvt_pk_fp8_f32 v192, v136, v140 op_sel:[0,0,1]
	v_cvt_pk_fp8_f32 v193, v144, v148
	v_cvt_pk_fp8_f32 v193, v152, v156 op_sel:[0,0,1]
	v_cvt_pk_fp8_f32 v194, v160, v164
	v_cvt_pk_fp8_f32 v194, v168, v172 op_sel:[0,0,1]
	v_cvt_pk_fp8_f32 v195, v176, v180
	v_cvt_pk_fp8_f32 v195, v184, v188 op_sel:[0,0,1]
	global_store_dwordx4 v209, v[192:195], s[24:25] sc1
	v_cvt_pk_fp8_f32 v196, v129, v133
	v_cvt_pk_fp8_f32 v196, v137, v141 op_sel:[0,0,1]
	v_cvt_pk_fp8_f32 v197, v145, v149
	v_cvt_pk_fp8_f32 v197, v153, v157 op_sel:[0,0,1]
	v_cvt_pk_fp8_f32 v198, v161, v165
	v_cvt_pk_fp8_f32 v198, v169, v173 op_sel:[0,0,1]
	v_cvt_pk_fp8_f32 v199, v177, v181
	v_cvt_pk_fp8_f32 v199, v185, v189 op_sel:[0,0,1]
	global_store_dwordx4 v209, v[196:199], s[24:25] offset:2048 sc1
	v_cvt_pk_fp8_f32 v200, v130, v134
	v_cvt_pk_fp8_f32 v200, v138, v142 op_sel:[0,0,1]
	v_cvt_pk_fp8_f32 v201, v146, v150
	v_cvt_pk_fp8_f32 v201, v154, v158 op_sel:[0,0,1]
	v_cvt_pk_fp8_f32 v202, v162, v166
	v_cvt_pk_fp8_f32 v202, v170, v174 op_sel:[0,0,1]
	v_cvt_pk_fp8_f32 v203, v178, v182
	v_cvt_pk_fp8_f32 v203, v186, v190 op_sel:[0,0,1]
	global_store_dwordx4 v209, v[200:203], s[26:27] sc1
	v_cvt_pk_fp8_f32 v204, v131, v135
	v_cvt_pk_fp8_f32 v204, v139, v143 op_sel:[0,0,1]
	v_cvt_pk_fp8_f32 v205, v147, v151
	v_cvt_pk_fp8_f32 v205, v155, v159 op_sel:[0,0,1]
	v_cvt_pk_fp8_f32 v206, v163, v167
	v_cvt_pk_fp8_f32 v206, v171, v175 op_sel:[0,0,1]
	v_cvt_pk_fp8_f32 v207, v179, v183
	v_cvt_pk_fp8_f32 v207, v187, v191 op_sel:[0,0,1]
	global_store_dwordx4 v209, v[204:207], s[26:27] offset:2048 sc1
	s_add_i32 s1, s21, 5
	s_and_b32 s1, s1, 15
	s_lshl_b32 s1, s1, 2
	s_add_i32 s1, s1, s20
	s_lshr_b32 s2, s1, 10
	s_and_b32 s4, s1, 0x3ff
	s_lshr_b32 s5, s4, 6
	s_and_b32 s4, s4, 63
	s_lshl_b32 s12, s2, 24
	s_lshl_b32 s13, s5, 20
	s_add_i32 s12, s12, s13
	s_lshl_b32 s13, s4, 7
	s_add_i32 s12, s12, s13
	s_add_u32 s14, s70, s12
	s_addc_u32 s15, s71, 0
	global_load_dwordx4 v[128:131], v208, s[14:15] sc1 nt
	s_add_u32 s18, s14, 0x2000
	s_addc_u32 s19, s15, 0
	global_load_dwordx4 v[132:135], v208, s[18:19] sc1 nt
	s_add_u32 s18, s14, 0x4000
	s_addc_u32 s19, s15, 0
	global_load_dwordx4 v[136:139], v208, s[18:19] sc1 nt
	s_add_u32 s18, s14, 0x6000
	s_addc_u32 s19, s15, 0
	global_load_dwordx4 v[140:143], v208, s[18:19] sc1 nt
	s_add_u32 s18, s14, 0x8000
	s_addc_u32 s19, s15, 0
	global_load_dwordx4 v[144:147], v208, s[18:19] sc1 nt
	s_add_u32 s18, s14, 0xa000
	s_addc_u32 s19, s15, 0
	global_load_dwordx4 v[148:151], v208, s[18:19] sc1 nt
	s_add_u32 s18, s14, 0xc000
	s_addc_u32 s19, s15, 0
	global_load_dwordx4 v[152:155], v208, s[18:19] sc1 nt
	s_add_u32 s18, s14, 0xe000
	s_addc_u32 s19, s15, 0
	global_load_dwordx4 v[156:159], v208, s[18:19] sc1 nt
	s_add_u32 s18, s14, 0x10000
	s_addc_u32 s19, s15, 0
	global_load_dwordx4 v[160:163], v208, s[18:19] sc1 nt
	s_add_u32 s18, s14, 0x12000
	s_addc_u32 s19, s15, 0
	global_load_dwordx4 v[164:167], v208, s[18:19] sc1 nt
	s_add_u32 s18, s14, 0x14000
	s_addc_u32 s19, s15, 0
	global_load_dwordx4 v[168:171], v208, s[18:19] sc1 nt
	s_add_u32 s18, s14, 0x16000
	s_addc_u32 s19, s15, 0
	global_load_dwordx4 v[172:175], v208, s[18:19] sc1 nt
	s_add_u32 s18, s14, 0x18000
	s_addc_u32 s19, s15, 0
	global_load_dwordx4 v[176:179], v208, s[18:19] sc1 nt
	s_add_u32 s18, s14, 0x1a000
	s_addc_u32 s19, s15, 0
	global_load_dwordx4 v[180:183], v208, s[18:19] sc1 nt
	s_add_u32 s18, s14, 0x1c000
	s_addc_u32 s19, s15, 0
	global_load_dwordx4 v[184:187], v208, s[18:19] sc1 nt
	s_add_u32 s18, s14, 0x1e000
	s_addc_u32 s19, s15, 0
	global_load_dwordx4 v[188:191], v208, s[18:19] sc1 nt
	s_waitcnt vmcnt(40)
	s_add_i32 s1, s21, 3
	s_and_b32 s1, s1, 15
	s_lshl_b32 s1, s1, 2
	s_add_i32 s1, s1, s20
	s_lshr_b32 s2, s1, 10
	s_and_b32 s4, s1, 0x3ff
	s_lshr_b32 s5, s4, 6
	s_and_b32 s4, s4, 63
	s_lshl_b32 s12, s2, 22
	s_lshl_b32 s13, s4, 16
	s_add_i32 s12, s12, s13
	s_lshl_b32 s13, s5, 7
	s_add_i32 s12, s12, s13
	s_add_u32 s24, s90, s12
	s_addc_u32 s25, s91, 0
	s_add_u32 s24, s24, 0x3b100000
	s_addc_u32 s25, s25, 0
	s_add_u32 s26, s24, 0x1000
	s_addc_u32 s27, s25, 0
	v_pk_mul_f32 v[0:1], v[0:1], s[16:17] op_sel_hi:[1,0]
	v_pk_mul_f32 v[2:3], v[2:3], s[16:17] op_sel_hi:[1,0]
	v_pk_mul_f32 v[4:5], v[4:5], s[16:17] op_sel_hi:[1,0]
	v_pk_mul_f32 v[6:7], v[6:7], s[16:17] op_sel_hi:[1,0]
	v_pk_mul_f32 v[8:9], v[8:9], s[16:17] op_sel_hi:[1,0]
	v_pk_mul_f32 v[10:11], v[10:11], s[16:17] op_sel_hi:[1,0]
	v_pk_mul_f32 v[12:13], v[12:13], s[16:17] op_sel_hi:[1,0]
	v_pk_mul_f32 v[14:15], v[14:15], s[16:17] op_sel_hi:[1,0]
	v_pk_mul_f32 v[16:17], v[16:17], s[16:17] op_sel_hi:[1,0]
	v_pk_mul_f32 v[18:19], v[18:19], s[16:17] op_sel_hi:[1,0]
	v_pk_mul_f32 v[20:21], v[20:21], s[16:17] op_sel_hi:[1,0]
	v_pk_mul_f32 v[22:23], v[22:23], s[16:17] op_sel_hi:[1,0]
	v_pk_mul_f32 v[24:25], v[24:25], s[16:17] op_sel_hi:[1,0]
	v_pk_mul_f32 v[26:27], v[26:27], s[16:17] op_sel_hi:[1,0]
	v_pk_mul_f32 v[28:29], v[28:29], s[16:17] op_sel_hi:[1,0]
	v_pk_mul_f32 v[30:31], v[30:31], s[16:17] op_sel_hi:[1,0]
	v_pk_mul_f32 v[32:33], v[32:33], s[16:17] op_sel_hi:[1,0]
	v_pk_mul_f32 v[34:35], v[34:35], s[16:17] op_sel_hi:[1,0]
	v_pk_mul_f32 v[36:37], v[36:37], s[16:17] op_sel_hi:[1,0]
	v_pk_mul_f32 v[38:39], v[38:39], s[16:17] op_sel_hi:[1,0]
	v_pk_mul_f32 v[40:41], v[40:41], s[16:17] op_sel_hi:[1,0]
	v_pk_mul_f32 v[42:43], v[42:43], s[16:17] op_sel_hi:[1,0]
	v_pk_mul_f32 v[44:45], v[44:45], s[16:17] op_sel_hi:[1,0]
	v_pk_mul_f32 v[46:47], v[46:47], s[16:17] op_sel_hi:[1,0]
	v_pk_mul_f32 v[48:49], v[48:49], s[16:17] op_sel_hi:[1,0]
	v_pk_mul_f32 v[50:51], v[50:51], s[16:17] op_sel_hi:[1,0]
	v_pk_mul_f32 v[52:53], v[52:53], s[16:17] op_sel_hi:[1,0]
	v_pk_mul_f32 v[54:55], v[54:55], s[16:17] op_sel_hi:[1,0]
	v_pk_mul_f32 v[56:57], v[56:57], s[16:17] op_sel_hi:[1,0]
	v_pk_mul_f32 v[58:59], v[58:59], s[16:17] op_sel_hi:[1,0]
	v_pk_mul_f32 v[60:61], v[60:61], s[16:17] op_sel_hi:[1,0]
	v_pk_mul_f32 v[62:63], v[62:63], s[16:17] op_sel_hi:[1,0]
	v_cvt_pk_fp8_f32 v192, v0, v4
	v_cvt_pk_fp8_f32 v192, v8, v12 op_sel:[0,0,1]
	v_cvt_pk_fp8_f32 v193, v16, v20
	v_cvt_pk_fp8_f32 v193, v24, v28 op_sel:[0,0,1]
	v_cvt_pk_fp8_f32 v194, v32, v36
	v_cvt_pk_fp8_f32 v194, v40, v44 op_sel:[0,0,1]
	v_cvt_pk_fp8_f32 v195, v48, v52
	v_cvt_pk_fp8_f32 v195, v56, v60 op_sel:[0,0,1]
	global_store_dwordx4 v209, v[192:195], s[24:25] sc1
	v_cvt_pk_fp8_f32 v196, v1, v5
	v_cvt_pk_fp8_f32 v196, v9, v13 op_sel:[0,0,1]
	v_cvt_pk_fp8_f32 v197, v17, v21
	v_cvt_pk_fp8_f32 v197, v25, v29 op_sel:[0,0,1]
	v_cvt_pk_fp8_f32 v198, v33, v37
	v_cvt_pk_fp8_f32 v198, v41, v45 op_sel:[0,0,1]
	v_cvt_pk_fp8_f32 v199, v49, v53
	v_cvt_pk_fp8_f32 v199, v57, v61 op_sel:[0,0,1]
	global_store_dwordx4 v209, v[196:199], s[24:25] offset:2048 sc1
	v_cvt_pk_fp8_f32 v200, v2, v6
	v_cvt_pk_fp8_f32 v200, v10, v14 op_sel:[0,0,1]
	v_cvt_pk_fp8_f32 v201, v18, v22
	v_cvt_pk_fp8_f32 v201, v26, v30 op_sel:[0,0,1]
	v_cvt_pk_fp8_f32 v202, v34, v38
	v_cvt_pk_fp8_f32 v202, v42, v46 op_sel:[0,0,1]
	v_cvt_pk_fp8_f32 v203, v50, v54
	v_cvt_pk_fp8_f32 v203, v58, v62 op_sel:[0,0,1]
	global_store_dwordx4 v209, v[200:203], s[26:27] sc1
	v_cvt_pk_fp8_f32 v204, v3, v7
	v_cvt_pk_fp8_f32 v204, v11, v15 op_sel:[0,0,1]
	v_cvt_pk_fp8_f32 v205, v19, v23
	v_cvt_pk_fp8_f32 v205, v27, v31 op_sel:[0,0,1]
	v_cvt_pk_fp8_f32 v206, v35, v39
	v_cvt_pk_fp8_f32 v206, v43, v47 op_sel:[0,0,1]
	v_cvt_pk_fp8_f32 v207, v51, v55
	v_cvt_pk_fp8_f32 v207, v59, v63 op_sel:[0,0,1]
	global_store_dwordx4 v209, v[204:207], s[26:27] offset:2048 sc1
	s_add_i32 s1, s21, 6
	s_and_b32 s1, s1, 15
	s_lshl_b32 s1, s1, 2
	s_add_i32 s1, s1, s20
	s_lshr_b32 s2, s1, 10
	s_and_b32 s4, s1, 0x3ff
	s_lshr_b32 s5, s4, 6
	s_and_b32 s4, s4, 63
	s_lshl_b32 s12, s2, 24
	s_lshl_b32 s13, s5, 20
	s_add_i32 s12, s12, s13
	s_lshl_b32 s13, s4, 7
	s_add_i32 s12, s12, s13
	s_add_u32 s14, s70, s12
	s_addc_u32 s15, s71, 0
	global_load_dwordx4 v[0:3], v208, s[14:15] sc1 nt
	s_add_u32 s18, s14, 0x2000
	s_addc_u32 s19, s15, 0
	global_load_dwordx4 v[4:7], v208, s[18:19] sc1 nt
	s_add_u32 s18, s14, 0x4000
	s_addc_u32 s19, s15, 0
	global_load_dwordx4 v[8:11], v208, s[18:19] sc1 nt
	s_add_u32 s18, s14, 0x6000
	s_addc_u32 s19, s15, 0
	global_load_dwordx4 v[12:15], v208, s[18:19] sc1 nt
	s_add_u32 s18, s14, 0x8000
	s_addc_u32 s19, s15, 0
	global_load_dwordx4 v[16:19], v208, s[18:19] sc1 nt
	s_add_u32 s18, s14, 0xa000
	s_addc_u32 s19, s15, 0
	global_load_dwordx4 v[20:23], v208, s[18:19] sc1 nt
	s_add_u32 s18, s14, 0xc000
	s_addc_u32 s19, s15, 0
	global_load_dwordx4 v[24:27], v208, s[18:19] sc1 nt
	s_add_u32 s18, s14, 0xe000
	s_addc_u32 s19, s15, 0
	global_load_dwordx4 v[28:31], v208, s[18:19] sc1 nt
	s_add_u32 s18, s14, 0x10000
	s_addc_u32 s19, s15, 0
	global_load_dwordx4 v[32:35], v208, s[18:19] sc1 nt
	s_add_u32 s18, s14, 0x12000
	s_addc_u32 s19, s15, 0
	global_load_dwordx4 v[36:39], v208, s[18:19] sc1 nt
	s_add_u32 s18, s14, 0x14000
	s_addc_u32 s19, s15, 0
	global_load_dwordx4 v[40:43], v208, s[18:19] sc1 nt
	s_add_u32 s18, s14, 0x16000
	s_addc_u32 s19, s15, 0
	global_load_dwordx4 v[44:47], v208, s[18:19] sc1 nt
	s_add_u32 s18, s14, 0x18000
	s_addc_u32 s19, s15, 0
	global_load_dwordx4 v[48:51], v208, s[18:19] sc1 nt
	s_add_u32 s18, s14, 0x1a000
	s_addc_u32 s19, s15, 0
	global_load_dwordx4 v[52:55], v208, s[18:19] sc1 nt
	s_add_u32 s18, s14, 0x1c000
	s_addc_u32 s19, s15, 0
	global_load_dwordx4 v[56:59], v208, s[18:19] sc1 nt
	s_add_u32 s18, s14, 0x1e000
	s_addc_u32 s19, s15, 0
	global_load_dwordx4 v[60:63], v208, s[18:19] sc1 nt
	s_waitcnt vmcnt(40)
	s_add_i32 s1, s21, 4
	s_and_b32 s1, s1, 15
	s_lshl_b32 s1, s1, 2
	s_add_i32 s1, s1, s20
	s_lshr_b32 s2, s1, 10
	s_and_b32 s4, s1, 0x3ff
	s_lshr_b32 s5, s4, 6
	s_and_b32 s4, s4, 63
	s_lshl_b32 s12, s2, 22
	s_lshl_b32 s13, s4, 16
	s_add_i32 s12, s12, s13
	s_lshl_b32 s13, s5, 7
	s_add_i32 s12, s12, s13
	s_add_u32 s24, s90, s12
	s_addc_u32 s25, s91, 0
	s_add_u32 s24, s24, 0x3b100000
	s_addc_u32 s25, s25, 0
	s_add_u32 s26, s24, 0x1000
	s_addc_u32 s27, s25, 0
	v_pk_mul_f32 v[64:65], v[64:65], s[16:17] op_sel_hi:[1,0]
	v_pk_mul_f32 v[66:67], v[66:67], s[16:17] op_sel_hi:[1,0]
	v_pk_mul_f32 v[68:69], v[68:69], s[16:17] op_sel_hi:[1,0]
	v_pk_mul_f32 v[70:71], v[70:71], s[16:17] op_sel_hi:[1,0]
	v_pk_mul_f32 v[72:73], v[72:73], s[16:17] op_sel_hi:[1,0]
	v_pk_mul_f32 v[74:75], v[74:75], s[16:17] op_sel_hi:[1,0]
	v_pk_mul_f32 v[76:77], v[76:77], s[16:17] op_sel_hi:[1,0]
	v_pk_mul_f32 v[78:79], v[78:79], s[16:17] op_sel_hi:[1,0]
	v_pk_mul_f32 v[80:81], v[80:81], s[16:17] op_sel_hi:[1,0]
	v_pk_mul_f32 v[82:83], v[82:83], s[16:17] op_sel_hi:[1,0]
	v_pk_mul_f32 v[84:85], v[84:85], s[16:17] op_sel_hi:[1,0]
	v_pk_mul_f32 v[86:87], v[86:87], s[16:17] op_sel_hi:[1,0]
	v_pk_mul_f32 v[88:89], v[88:89], s[16:17] op_sel_hi:[1,0]
	v_pk_mul_f32 v[90:91], v[90:91], s[16:17] op_sel_hi:[1,0]
	v_pk_mul_f32 v[92:93], v[92:93], s[16:17] op_sel_hi:[1,0]
	v_pk_mul_f32 v[94:95], v[94:95], s[16:17] op_sel_hi:[1,0]
	v_pk_mul_f32 v[96:97], v[96:97], s[16:17] op_sel_hi:[1,0]
	v_pk_mul_f32 v[98:99], v[98:99], s[16:17] op_sel_hi:[1,0]
	v_pk_mul_f32 v[100:101], v[100:101], s[16:17] op_sel_hi:[1,0]
	v_pk_mul_f32 v[102:103], v[102:103], s[16:17] op_sel_hi:[1,0]
	v_pk_mul_f32 v[104:105], v[104:105], s[16:17] op_sel_hi:[1,0]
	v_pk_mul_f32 v[106:107], v[106:107], s[16:17] op_sel_hi:[1,0]
	v_pk_mul_f32 v[108:109], v[108:109], s[16:17] op_sel_hi:[1,0]
	v_pk_mul_f32 v[110:111], v[110:111], s[16:17] op_sel_hi:[1,0]
	v_pk_mul_f32 v[112:113], v[112:113], s[16:17] op_sel_hi:[1,0]
	v_pk_mul_f32 v[114:115], v[114:115], s[16:17] op_sel_hi:[1,0]
	v_pk_mul_f32 v[116:117], v[116:117], s[16:17] op_sel_hi:[1,0]
	v_pk_mul_f32 v[118:119], v[118:119], s[16:17] op_sel_hi:[1,0]
	v_pk_mul_f32 v[120:121], v[120:121], s[16:17] op_sel_hi:[1,0]
	v_pk_mul_f32 v[122:123], v[122:123], s[16:17] op_sel_hi:[1,0]
	v_pk_mul_f32 v[124:125], v[124:125], s[16:17] op_sel_hi:[1,0]
	v_pk_mul_f32 v[126:127], v[126:127], s[16:17] op_sel_hi:[1,0]
	v_cvt_pk_fp8_f32 v192, v64, v68
	v_cvt_pk_fp8_f32 v192, v72, v76 op_sel:[0,0,1]
	v_cvt_pk_fp8_f32 v193, v80, v84
	v_cvt_pk_fp8_f32 v193, v88, v92 op_sel:[0,0,1]
	v_cvt_pk_fp8_f32 v194, v96, v100
	v_cvt_pk_fp8_f32 v194, v104, v108 op_sel:[0,0,1]
	v_cvt_pk_fp8_f32 v195, v112, v116
	v_cvt_pk_fp8_f32 v195, v120, v124 op_sel:[0,0,1]
	global_store_dwordx4 v209, v[192:195], s[24:25] sc1
	v_cvt_pk_fp8_f32 v196, v65, v69
	v_cvt_pk_fp8_f32 v196, v73, v77 op_sel:[0,0,1]
	v_cvt_pk_fp8_f32 v197, v81, v85
	v_cvt_pk_fp8_f32 v197, v89, v93 op_sel:[0,0,1]
	v_cvt_pk_fp8_f32 v198, v97, v101
	v_cvt_pk_fp8_f32 v198, v105, v109 op_sel:[0,0,1]
	v_cvt_pk_fp8_f32 v199, v113, v117
	v_cvt_pk_fp8_f32 v199, v121, v125 op_sel:[0,0,1]
	global_store_dwordx4 v209, v[196:199], s[24:25] offset:2048 sc1
	v_cvt_pk_fp8_f32 v200, v66, v70
	v_cvt_pk_fp8_f32 v200, v74, v78 op_sel:[0,0,1]
	v_cvt_pk_fp8_f32 v201, v82, v86
	v_cvt_pk_fp8_f32 v201, v90, v94 op_sel:[0,0,1]
	v_cvt_pk_fp8_f32 v202, v98, v102
	v_cvt_pk_fp8_f32 v202, v106, v110 op_sel:[0,0,1]
	v_cvt_pk_fp8_f32 v203, v114, v118
	v_cvt_pk_fp8_f32 v203, v122, v126 op_sel:[0,0,1]
	global_store_dwordx4 v209, v[200:203], s[26:27] sc1
	v_cvt_pk_fp8_f32 v204, v67, v71
	v_cvt_pk_fp8_f32 v204, v75, v79 op_sel:[0,0,1]
	v_cvt_pk_fp8_f32 v205, v83, v87
	v_cvt_pk_fp8_f32 v205, v91, v95 op_sel:[0,0,1]
	v_cvt_pk_fp8_f32 v206, v99, v103
	v_cvt_pk_fp8_f32 v206, v107, v111 op_sel:[0,0,1]
	v_cvt_pk_fp8_f32 v207, v115, v119
	v_cvt_pk_fp8_f32 v207, v123, v127 op_sel:[0,0,1]
	global_store_dwordx4 v209, v[204:207], s[26:27] offset:2048 sc1
	s_add_i32 s1, s21, 7
	s_and_b32 s1, s1, 15
	s_lshl_b32 s1, s1, 2
	s_add_i32 s1, s1, s20
	s_lshr_b32 s2, s1, 10
	s_and_b32 s4, s1, 0x3ff
	s_lshr_b32 s5, s4, 6
	s_and_b32 s4, s4, 63
	s_lshl_b32 s12, s2, 24
	s_lshl_b32 s13, s5, 20
	s_add_i32 s12, s12, s13
	s_lshl_b32 s13, s4, 7
	s_add_i32 s12, s12, s13
	s_add_u32 s14, s70, s12
	s_addc_u32 s15, s71, 0
	global_load_dwordx4 v[64:67], v208, s[14:15] sc1 nt
	s_add_u32 s18, s14, 0x2000
	s_addc_u32 s19, s15, 0
	global_load_dwordx4 v[68:71], v208, s[18:19] sc1 nt
	s_add_u32 s18, s14, 0x4000
	s_addc_u32 s19, s15, 0
	global_load_dwordx4 v[72:75], v208, s[18:19] sc1 nt
	s_add_u32 s18, s14, 0x6000
	s_addc_u32 s19, s15, 0
	global_load_dwordx4 v[76:79], v208, s[18:19] sc1 nt
	s_add_u32 s18, s14, 0x8000
	s_addc_u32 s19, s15, 0
	global_load_dwordx4 v[80:83], v208, s[18:19] sc1 nt
	s_add_u32 s18, s14, 0xa000
	s_addc_u32 s19, s15, 0
	global_load_dwordx4 v[84:87], v208, s[18:19] sc1 nt
	s_add_u32 s18, s14, 0xc000
	s_addc_u32 s19, s15, 0
	global_load_dwordx4 v[88:91], v208, s[18:19] sc1 nt
	s_add_u32 s18, s14, 0xe000
	s_addc_u32 s19, s15, 0
	global_load_dwordx4 v[92:95], v208, s[18:19] sc1 nt
	s_add_u32 s18, s14, 0x10000
	s_addc_u32 s19, s15, 0
	global_load_dwordx4 v[96:99], v208, s[18:19] sc1 nt
	s_add_u32 s18, s14, 0x12000
	s_addc_u32 s19, s15, 0
	global_load_dwordx4 v[100:103], v208, s[18:19] sc1 nt
	s_add_u32 s18, s14, 0x14000
	s_addc_u32 s19, s15, 0
	global_load_dwordx4 v[104:107], v208, s[18:19] sc1 nt
	s_add_u32 s18, s14, 0x16000
	s_addc_u32 s19, s15, 0
	global_load_dwordx4 v[108:111], v208, s[18:19] sc1 nt
	s_add_u32 s18, s14, 0x18000
	s_addc_u32 s19, s15, 0
	global_load_dwordx4 v[112:115], v208, s[18:19] sc1 nt
	s_add_u32 s18, s14, 0x1a000
	s_addc_u32 s19, s15, 0
	global_load_dwordx4 v[116:119], v208, s[18:19] sc1 nt
	s_add_u32 s18, s14, 0x1c000
	s_addc_u32 s19, s15, 0
	global_load_dwordx4 v[120:123], v208, s[18:19] sc1 nt
	s_add_u32 s18, s14, 0x1e000
	s_addc_u32 s19, s15, 0
	global_load_dwordx4 v[124:127], v208, s[18:19] sc1 nt
	s_waitcnt vmcnt(40)
	s_add_i32 s1, s21, 5
	s_and_b32 s1, s1, 15
	s_lshl_b32 s1, s1, 2
	s_add_i32 s1, s1, s20
	s_lshr_b32 s2, s1, 10
	s_and_b32 s4, s1, 0x3ff
	s_lshr_b32 s5, s4, 6
	s_and_b32 s4, s4, 63
	s_lshl_b32 s12, s2, 22
	s_lshl_b32 s13, s4, 16
	s_add_i32 s12, s12, s13
	s_lshl_b32 s13, s5, 7
	s_add_i32 s12, s12, s13
	s_add_u32 s24, s90, s12
	s_addc_u32 s25, s91, 0
	s_add_u32 s24, s24, 0x3b100000
	s_addc_u32 s25, s25, 0
	s_add_u32 s26, s24, 0x1000
	s_addc_u32 s27, s25, 0
	v_pk_mul_f32 v[128:129], v[128:129], s[16:17] op_sel_hi:[1,0]
	v_pk_mul_f32 v[130:131], v[130:131], s[16:17] op_sel_hi:[1,0]
	v_pk_mul_f32 v[132:133], v[132:133], s[16:17] op_sel_hi:[1,0]
	v_pk_mul_f32 v[134:135], v[134:135], s[16:17] op_sel_hi:[1,0]
	v_pk_mul_f32 v[136:137], v[136:137], s[16:17] op_sel_hi:[1,0]
	v_pk_mul_f32 v[138:139], v[138:139], s[16:17] op_sel_hi:[1,0]
	v_pk_mul_f32 v[140:141], v[140:141], s[16:17] op_sel_hi:[1,0]
	v_pk_mul_f32 v[142:143], v[142:143], s[16:17] op_sel_hi:[1,0]
	v_pk_mul_f32 v[144:145], v[144:145], s[16:17] op_sel_hi:[1,0]
	v_pk_mul_f32 v[146:147], v[146:147], s[16:17] op_sel_hi:[1,0]
	v_pk_mul_f32 v[148:149], v[148:149], s[16:17] op_sel_hi:[1,0]
	v_pk_mul_f32 v[150:151], v[150:151], s[16:17] op_sel_hi:[1,0]
	v_pk_mul_f32 v[152:153], v[152:153], s[16:17] op_sel_hi:[1,0]
	v_pk_mul_f32 v[154:155], v[154:155], s[16:17] op_sel_hi:[1,0]
	v_pk_mul_f32 v[156:157], v[156:157], s[16:17] op_sel_hi:[1,0]
	v_pk_mul_f32 v[158:159], v[158:159], s[16:17] op_sel_hi:[1,0]
	v_pk_mul_f32 v[160:161], v[160:161], s[16:17] op_sel_hi:[1,0]
	v_pk_mul_f32 v[162:163], v[162:163], s[16:17] op_sel_hi:[1,0]
	v_pk_mul_f32 v[164:165], v[164:165], s[16:17] op_sel_hi:[1,0]
	v_pk_mul_f32 v[166:167], v[166:167], s[16:17] op_sel_hi:[1,0]
	v_pk_mul_f32 v[168:169], v[168:169], s[16:17] op_sel_hi:[1,0]
	v_pk_mul_f32 v[170:171], v[170:171], s[16:17] op_sel_hi:[1,0]
	v_pk_mul_f32 v[172:173], v[172:173], s[16:17] op_sel_hi:[1,0]
	v_pk_mul_f32 v[174:175], v[174:175], s[16:17] op_sel_hi:[1,0]
	v_pk_mul_f32 v[176:177], v[176:177], s[16:17] op_sel_hi:[1,0]
	v_pk_mul_f32 v[178:179], v[178:179], s[16:17] op_sel_hi:[1,0]
	v_pk_mul_f32 v[180:181], v[180:181], s[16:17] op_sel_hi:[1,0]
	v_pk_mul_f32 v[182:183], v[182:183], s[16:17] op_sel_hi:[1,0]
	v_pk_mul_f32 v[184:185], v[184:185], s[16:17] op_sel_hi:[1,0]
	v_pk_mul_f32 v[186:187], v[186:187], s[16:17] op_sel_hi:[1,0]
	v_pk_mul_f32 v[188:189], v[188:189], s[16:17] op_sel_hi:[1,0]
	v_pk_mul_f32 v[190:191], v[190:191], s[16:17] op_sel_hi:[1,0]
	v_cvt_pk_fp8_f32 v192, v128, v132
	v_cvt_pk_fp8_f32 v192, v136, v140 op_sel:[0,0,1]
	v_cvt_pk_fp8_f32 v193, v144, v148
	v_cvt_pk_fp8_f32 v193, v152, v156 op_sel:[0,0,1]
	v_cvt_pk_fp8_f32 v194, v160, v164
	v_cvt_pk_fp8_f32 v194, v168, v172 op_sel:[0,0,1]
	v_cvt_pk_fp8_f32 v195, v176, v180
	v_cvt_pk_fp8_f32 v195, v184, v188 op_sel:[0,0,1]
	global_store_dwordx4 v209, v[192:195], s[24:25] sc1
	v_cvt_pk_fp8_f32 v196, v129, v133
	v_cvt_pk_fp8_f32 v196, v137, v141 op_sel:[0,0,1]
	v_cvt_pk_fp8_f32 v197, v145, v149
	v_cvt_pk_fp8_f32 v197, v153, v157 op_sel:[0,0,1]
	v_cvt_pk_fp8_f32 v198, v161, v165
	v_cvt_pk_fp8_f32 v198, v169, v173 op_sel:[0,0,1]
	v_cvt_pk_fp8_f32 v199, v177, v181
	v_cvt_pk_fp8_f32 v199, v185, v189 op_sel:[0,0,1]
	global_store_dwordx4 v209, v[196:199], s[24:25] offset:2048 sc1
	v_cvt_pk_fp8_f32 v200, v130, v134
	v_cvt_pk_fp8_f32 v200, v138, v142 op_sel:[0,0,1]
	v_cvt_pk_fp8_f32 v201, v146, v150
	v_cvt_pk_fp8_f32 v201, v154, v158 op_sel:[0,0,1]
	v_cvt_pk_fp8_f32 v202, v162, v166
	v_cvt_pk_fp8_f32 v202, v170, v174 op_sel:[0,0,1]
	v_cvt_pk_fp8_f32 v203, v178, v182
	v_cvt_pk_fp8_f32 v203, v186, v190 op_sel:[0,0,1]
	global_store_dwordx4 v209, v[200:203], s[26:27] sc1
	v_cvt_pk_fp8_f32 v204, v131, v135
	v_cvt_pk_fp8_f32 v204, v139, v143 op_sel:[0,0,1]
	v_cvt_pk_fp8_f32 v205, v147, v151
	v_cvt_pk_fp8_f32 v205, v155, v159 op_sel:[0,0,1]
	v_cvt_pk_fp8_f32 v206, v163, v167
	v_cvt_pk_fp8_f32 v206, v171, v175 op_sel:[0,0,1]
	v_cvt_pk_fp8_f32 v207, v179, v183
	v_cvt_pk_fp8_f32 v207, v187, v191 op_sel:[0,0,1]
	global_store_dwordx4 v209, v[204:207], s[26:27] offset:2048 sc1
	s_add_i32 s1, s21, 8
	s_and_b32 s1, s1, 15
	s_lshl_b32 s1, s1, 2
	s_add_i32 s1, s1, s20
	s_lshr_b32 s2, s1, 10
	s_and_b32 s4, s1, 0x3ff
	s_lshr_b32 s5, s4, 6
	s_and_b32 s4, s4, 63
	s_lshl_b32 s12, s2, 24
	s_lshl_b32 s13, s5, 20
	s_add_i32 s12, s12, s13
	s_lshl_b32 s13, s4, 7
	s_add_i32 s12, s12, s13
	s_add_u32 s14, s70, s12
	s_addc_u32 s15, s71, 0
	global_load_dwordx4 v[128:131], v208, s[14:15] sc1 nt
	s_add_u32 s18, s14, 0x2000
	s_addc_u32 s19, s15, 0
	global_load_dwordx4 v[132:135], v208, s[18:19] sc1 nt
	s_add_u32 s18, s14, 0x4000
	s_addc_u32 s19, s15, 0
	global_load_dwordx4 v[136:139], v208, s[18:19] sc1 nt
	s_add_u32 s18, s14, 0x6000
	s_addc_u32 s19, s15, 0
	global_load_dwordx4 v[140:143], v208, s[18:19] sc1 nt
	s_add_u32 s18, s14, 0x8000
	s_addc_u32 s19, s15, 0
	global_load_dwordx4 v[144:147], v208, s[18:19] sc1 nt
	s_add_u32 s18, s14, 0xa000
	s_addc_u32 s19, s15, 0
	global_load_dwordx4 v[148:151], v208, s[18:19] sc1 nt
	s_add_u32 s18, s14, 0xc000
	s_addc_u32 s19, s15, 0
	global_load_dwordx4 v[152:155], v208, s[18:19] sc1 nt
	s_add_u32 s18, s14, 0xe000
	s_addc_u32 s19, s15, 0
	global_load_dwordx4 v[156:159], v208, s[18:19] sc1 nt
	s_add_u32 s18, s14, 0x10000
	s_addc_u32 s19, s15, 0
	global_load_dwordx4 v[160:163], v208, s[18:19] sc1 nt
	s_add_u32 s18, s14, 0x12000
	s_addc_u32 s19, s15, 0
	global_load_dwordx4 v[164:167], v208, s[18:19] sc1 nt
	s_add_u32 s18, s14, 0x14000
	s_addc_u32 s19, s15, 0
	global_load_dwordx4 v[168:171], v208, s[18:19] sc1 nt
	s_add_u32 s18, s14, 0x16000
	s_addc_u32 s19, s15, 0
	global_load_dwordx4 v[172:175], v208, s[18:19] sc1 nt
	s_add_u32 s18, s14, 0x18000
	s_addc_u32 s19, s15, 0
	global_load_dwordx4 v[176:179], v208, s[18:19] sc1 nt
	s_add_u32 s18, s14, 0x1a000
	s_addc_u32 s19, s15, 0
	global_load_dwordx4 v[180:183], v208, s[18:19] sc1 nt
	s_add_u32 s18, s14, 0x1c000
	s_addc_u32 s19, s15, 0
	global_load_dwordx4 v[184:187], v208, s[18:19] sc1 nt
	s_add_u32 s18, s14, 0x1e000
	s_addc_u32 s19, s15, 0
	global_load_dwordx4 v[188:191], v208, s[18:19] sc1 nt
	s_waitcnt vmcnt(40)
	s_add_i32 s1, s21, 6
	s_and_b32 s1, s1, 15
	s_lshl_b32 s1, s1, 2
	s_add_i32 s1, s1, s20
	s_lshr_b32 s2, s1, 10
	s_and_b32 s4, s1, 0x3ff
	s_lshr_b32 s5, s4, 6
	s_and_b32 s4, s4, 63
	s_lshl_b32 s12, s2, 22
	s_lshl_b32 s13, s4, 16
	s_add_i32 s12, s12, s13
	s_lshl_b32 s13, s5, 7
	s_add_i32 s12, s12, s13
	s_add_u32 s24, s90, s12
	s_addc_u32 s25, s91, 0
	s_add_u32 s24, s24, 0x3b100000
	s_addc_u32 s25, s25, 0
	s_add_u32 s26, s24, 0x1000
	s_addc_u32 s27, s25, 0
	v_pk_mul_f32 v[0:1], v[0:1], s[16:17] op_sel_hi:[1,0]
	v_pk_mul_f32 v[2:3], v[2:3], s[16:17] op_sel_hi:[1,0]
	v_pk_mul_f32 v[4:5], v[4:5], s[16:17] op_sel_hi:[1,0]
	v_pk_mul_f32 v[6:7], v[6:7], s[16:17] op_sel_hi:[1,0]
	v_pk_mul_f32 v[8:9], v[8:9], s[16:17] op_sel_hi:[1,0]
	v_pk_mul_f32 v[10:11], v[10:11], s[16:17] op_sel_hi:[1,0]
	v_pk_mul_f32 v[12:13], v[12:13], s[16:17] op_sel_hi:[1,0]
	v_pk_mul_f32 v[14:15], v[14:15], s[16:17] op_sel_hi:[1,0]
	v_pk_mul_f32 v[16:17], v[16:17], s[16:17] op_sel_hi:[1,0]
	v_pk_mul_f32 v[18:19], v[18:19], s[16:17] op_sel_hi:[1,0]
	v_pk_mul_f32 v[20:21], v[20:21], s[16:17] op_sel_hi:[1,0]
	v_pk_mul_f32 v[22:23], v[22:23], s[16:17] op_sel_hi:[1,0]
	v_pk_mul_f32 v[24:25], v[24:25], s[16:17] op_sel_hi:[1,0]
	v_pk_mul_f32 v[26:27], v[26:27], s[16:17] op_sel_hi:[1,0]
	v_pk_mul_f32 v[28:29], v[28:29], s[16:17] op_sel_hi:[1,0]
	v_pk_mul_f32 v[30:31], v[30:31], s[16:17] op_sel_hi:[1,0]
	v_pk_mul_f32 v[32:33], v[32:33], s[16:17] op_sel_hi:[1,0]
	v_pk_mul_f32 v[34:35], v[34:35], s[16:17] op_sel_hi:[1,0]
	v_pk_mul_f32 v[36:37], v[36:37], s[16:17] op_sel_hi:[1,0]
	v_pk_mul_f32 v[38:39], v[38:39], s[16:17] op_sel_hi:[1,0]
	v_pk_mul_f32 v[40:41], v[40:41], s[16:17] op_sel_hi:[1,0]
	v_pk_mul_f32 v[42:43], v[42:43], s[16:17] op_sel_hi:[1,0]
	v_pk_mul_f32 v[44:45], v[44:45], s[16:17] op_sel_hi:[1,0]
	v_pk_mul_f32 v[46:47], v[46:47], s[16:17] op_sel_hi:[1,0]
	v_pk_mul_f32 v[48:49], v[48:49], s[16:17] op_sel_hi:[1,0]
	v_pk_mul_f32 v[50:51], v[50:51], s[16:17] op_sel_hi:[1,0]
	v_pk_mul_f32 v[52:53], v[52:53], s[16:17] op_sel_hi:[1,0]
	v_pk_mul_f32 v[54:55], v[54:55], s[16:17] op_sel_hi:[1,0]
	v_pk_mul_f32 v[56:57], v[56:57], s[16:17] op_sel_hi:[1,0]
	v_pk_mul_f32 v[58:59], v[58:59], s[16:17] op_sel_hi:[1,0]
	v_pk_mul_f32 v[60:61], v[60:61], s[16:17] op_sel_hi:[1,0]
	v_pk_mul_f32 v[62:63], v[62:63], s[16:17] op_sel_hi:[1,0]
	v_cvt_pk_fp8_f32 v192, v0, v4
	v_cvt_pk_fp8_f32 v192, v8, v12 op_sel:[0,0,1]
	v_cvt_pk_fp8_f32 v193, v16, v20
	v_cvt_pk_fp8_f32 v193, v24, v28 op_sel:[0,0,1]
	v_cvt_pk_fp8_f32 v194, v32, v36
	v_cvt_pk_fp8_f32 v194, v40, v44 op_sel:[0,0,1]
	v_cvt_pk_fp8_f32 v195, v48, v52
	v_cvt_pk_fp8_f32 v195, v56, v60 op_sel:[0,0,1]
	global_store_dwordx4 v209, v[192:195], s[24:25] sc1
	v_cvt_pk_fp8_f32 v196, v1, v5
	v_cvt_pk_fp8_f32 v196, v9, v13 op_sel:[0,0,1]
	v_cvt_pk_fp8_f32 v197, v17, v21
	v_cvt_pk_fp8_f32 v197, v25, v29 op_sel:[0,0,1]
	v_cvt_pk_fp8_f32 v198, v33, v37
	v_cvt_pk_fp8_f32 v198, v41, v45 op_sel:[0,0,1]
	v_cvt_pk_fp8_f32 v199, v49, v53
	v_cvt_pk_fp8_f32 v199, v57, v61 op_sel:[0,0,1]
	global_store_dwordx4 v209, v[196:199], s[24:25] offset:2048 sc1
	v_cvt_pk_fp8_f32 v200, v2, v6
	v_cvt_pk_fp8_f32 v200, v10, v14 op_sel:[0,0,1]
	v_cvt_pk_fp8_f32 v201, v18, v22
	v_cvt_pk_fp8_f32 v201, v26, v30 op_sel:[0,0,1]
	v_cvt_pk_fp8_f32 v202, v34, v38
	v_cvt_pk_fp8_f32 v202, v42, v46 op_sel:[0,0,1]
	v_cvt_pk_fp8_f32 v203, v50, v54
	v_cvt_pk_fp8_f32 v203, v58, v62 op_sel:[0,0,1]
	global_store_dwordx4 v209, v[200:203], s[26:27] sc1
	v_cvt_pk_fp8_f32 v204, v3, v7
	v_cvt_pk_fp8_f32 v204, v11, v15 op_sel:[0,0,1]
	v_cvt_pk_fp8_f32 v205, v19, v23
	v_cvt_pk_fp8_f32 v205, v27, v31 op_sel:[0,0,1]
	v_cvt_pk_fp8_f32 v206, v35, v39
	v_cvt_pk_fp8_f32 v206, v43, v47 op_sel:[0,0,1]
	v_cvt_pk_fp8_f32 v207, v51, v55
	v_cvt_pk_fp8_f32 v207, v59, v63 op_sel:[0,0,1]
	global_store_dwordx4 v209, v[204:207], s[26:27] offset:2048 sc1
	s_add_i32 s1, s21, 9
	s_and_b32 s1, s1, 15
	s_lshl_b32 s1, s1, 2
	s_add_i32 s1, s1, s20
	s_lshr_b32 s2, s1, 10
	s_and_b32 s4, s1, 0x3ff
	s_lshr_b32 s5, s4, 6
	s_and_b32 s4, s4, 63
	s_lshl_b32 s12, s2, 24
	s_lshl_b32 s13, s5, 20
	s_add_i32 s12, s12, s13
	s_lshl_b32 s13, s4, 7
	s_add_i32 s12, s12, s13
	s_add_u32 s14, s70, s12
	s_addc_u32 s15, s71, 0
	global_load_dwordx4 v[0:3], v208, s[14:15] sc1 nt
	s_add_u32 s18, s14, 0x2000
	s_addc_u32 s19, s15, 0
	global_load_dwordx4 v[4:7], v208, s[18:19] sc1 nt
	s_add_u32 s18, s14, 0x4000
	s_addc_u32 s19, s15, 0
	global_load_dwordx4 v[8:11], v208, s[18:19] sc1 nt
	s_add_u32 s18, s14, 0x6000
	s_addc_u32 s19, s15, 0
	global_load_dwordx4 v[12:15], v208, s[18:19] sc1 nt
	s_add_u32 s18, s14, 0x8000
	s_addc_u32 s19, s15, 0
	global_load_dwordx4 v[16:19], v208, s[18:19] sc1 nt
	s_add_u32 s18, s14, 0xa000
	s_addc_u32 s19, s15, 0
	global_load_dwordx4 v[20:23], v208, s[18:19] sc1 nt
	s_add_u32 s18, s14, 0xc000
	s_addc_u32 s19, s15, 0
	global_load_dwordx4 v[24:27], v208, s[18:19] sc1 nt
	s_add_u32 s18, s14, 0xe000
	s_addc_u32 s19, s15, 0
	global_load_dwordx4 v[28:31], v208, s[18:19] sc1 nt
	s_add_u32 s18, s14, 0x10000
	s_addc_u32 s19, s15, 0
	global_load_dwordx4 v[32:35], v208, s[18:19] sc1 nt
	s_add_u32 s18, s14, 0x12000
	s_addc_u32 s19, s15, 0
	global_load_dwordx4 v[36:39], v208, s[18:19] sc1 nt
	s_add_u32 s18, s14, 0x14000
	s_addc_u32 s19, s15, 0
	global_load_dwordx4 v[40:43], v208, s[18:19] sc1 nt
	s_add_u32 s18, s14, 0x16000
	s_addc_u32 s19, s15, 0
	global_load_dwordx4 v[44:47], v208, s[18:19] sc1 nt
	s_add_u32 s18, s14, 0x18000
	s_addc_u32 s19, s15, 0
	global_load_dwordx4 v[48:51], v208, s[18:19] sc1 nt
	s_add_u32 s18, s14, 0x1a000
	s_addc_u32 s19, s15, 0
	global_load_dwordx4 v[52:55], v208, s[18:19] sc1 nt
	s_add_u32 s18, s14, 0x1c000
	s_addc_u32 s19, s15, 0
	global_load_dwordx4 v[56:59], v208, s[18:19] sc1 nt
	s_add_u32 s18, s14, 0x1e000
	s_addc_u32 s19, s15, 0
	global_load_dwordx4 v[60:63], v208, s[18:19] sc1 nt
	s_waitcnt vmcnt(40)
	s_add_i32 s1, s21, 7
	s_and_b32 s1, s1, 15
	s_lshl_b32 s1, s1, 2
	s_add_i32 s1, s1, s20
	s_lshr_b32 s2, s1, 10
	s_and_b32 s4, s1, 0x3ff
	s_lshr_b32 s5, s4, 6
	s_and_b32 s4, s4, 63
	s_lshl_b32 s12, s2, 22
	s_lshl_b32 s13, s4, 16
	s_add_i32 s12, s12, s13
	s_lshl_b32 s13, s5, 7
	s_add_i32 s12, s12, s13
	s_add_u32 s24, s90, s12
	s_addc_u32 s25, s91, 0
	s_add_u32 s24, s24, 0x3b100000
	s_addc_u32 s25, s25, 0
	s_add_u32 s26, s24, 0x1000
	s_addc_u32 s27, s25, 0
	v_pk_mul_f32 v[64:65], v[64:65], s[16:17] op_sel_hi:[1,0]
	v_pk_mul_f32 v[66:67], v[66:67], s[16:17] op_sel_hi:[1,0]
	v_pk_mul_f32 v[68:69], v[68:69], s[16:17] op_sel_hi:[1,0]
	v_pk_mul_f32 v[70:71], v[70:71], s[16:17] op_sel_hi:[1,0]
	v_pk_mul_f32 v[72:73], v[72:73], s[16:17] op_sel_hi:[1,0]
	v_pk_mul_f32 v[74:75], v[74:75], s[16:17] op_sel_hi:[1,0]
	v_pk_mul_f32 v[76:77], v[76:77], s[16:17] op_sel_hi:[1,0]
	v_pk_mul_f32 v[78:79], v[78:79], s[16:17] op_sel_hi:[1,0]
	v_pk_mul_f32 v[80:81], v[80:81], s[16:17] op_sel_hi:[1,0]
	v_pk_mul_f32 v[82:83], v[82:83], s[16:17] op_sel_hi:[1,0]
	v_pk_mul_f32 v[84:85], v[84:85], s[16:17] op_sel_hi:[1,0]
	v_pk_mul_f32 v[86:87], v[86:87], s[16:17] op_sel_hi:[1,0]
	v_pk_mul_f32 v[88:89], v[88:89], s[16:17] op_sel_hi:[1,0]
	v_pk_mul_f32 v[90:91], v[90:91], s[16:17] op_sel_hi:[1,0]
	v_pk_mul_f32 v[92:93], v[92:93], s[16:17] op_sel_hi:[1,0]
	v_pk_mul_f32 v[94:95], v[94:95], s[16:17] op_sel_hi:[1,0]
	v_pk_mul_f32 v[96:97], v[96:97], s[16:17] op_sel_hi:[1,0]
	v_pk_mul_f32 v[98:99], v[98:99], s[16:17] op_sel_hi:[1,0]
	v_pk_mul_f32 v[100:101], v[100:101], s[16:17] op_sel_hi:[1,0]
	v_pk_mul_f32 v[102:103], v[102:103], s[16:17] op_sel_hi:[1,0]
	v_pk_mul_f32 v[104:105], v[104:105], s[16:17] op_sel_hi:[1,0]
	v_pk_mul_f32 v[106:107], v[106:107], s[16:17] op_sel_hi:[1,0]
	v_pk_mul_f32 v[108:109], v[108:109], s[16:17] op_sel_hi:[1,0]
	v_pk_mul_f32 v[110:111], v[110:111], s[16:17] op_sel_hi:[1,0]
	v_pk_mul_f32 v[112:113], v[112:113], s[16:17] op_sel_hi:[1,0]
	v_pk_mul_f32 v[114:115], v[114:115], s[16:17] op_sel_hi:[1,0]
	v_pk_mul_f32 v[116:117], v[116:117], s[16:17] op_sel_hi:[1,0]
	v_pk_mul_f32 v[118:119], v[118:119], s[16:17] op_sel_hi:[1,0]
	v_pk_mul_f32 v[120:121], v[120:121], s[16:17] op_sel_hi:[1,0]
	v_pk_mul_f32 v[122:123], v[122:123], s[16:17] op_sel_hi:[1,0]
	v_pk_mul_f32 v[124:125], v[124:125], s[16:17] op_sel_hi:[1,0]
	v_pk_mul_f32 v[126:127], v[126:127], s[16:17] op_sel_hi:[1,0]
	v_cvt_pk_fp8_f32 v192, v64, v68
	v_cvt_pk_fp8_f32 v192, v72, v76 op_sel:[0,0,1]
	v_cvt_pk_fp8_f32 v193, v80, v84
	v_cvt_pk_fp8_f32 v193, v88, v92 op_sel:[0,0,1]
	v_cvt_pk_fp8_f32 v194, v96, v100
	v_cvt_pk_fp8_f32 v194, v104, v108 op_sel:[0,0,1]
	v_cvt_pk_fp8_f32 v195, v112, v116
	v_cvt_pk_fp8_f32 v195, v120, v124 op_sel:[0,0,1]
	global_store_dwordx4 v209, v[192:195], s[24:25] sc1
	v_cvt_pk_fp8_f32 v196, v65, v69
	v_cvt_pk_fp8_f32 v196, v73, v77 op_sel:[0,0,1]
	v_cvt_pk_fp8_f32 v197, v81, v85
	v_cvt_pk_fp8_f32 v197, v89, v93 op_sel:[0,0,1]
	v_cvt_pk_fp8_f32 v198, v97, v101
	v_cvt_pk_fp8_f32 v198, v105, v109 op_sel:[0,0,1]
	v_cvt_pk_fp8_f32 v199, v113, v117
	v_cvt_pk_fp8_f32 v199, v121, v125 op_sel:[0,0,1]
	global_store_dwordx4 v209, v[196:199], s[24:25] offset:2048 sc1
	v_cvt_pk_fp8_f32 v200, v66, v70
	v_cvt_pk_fp8_f32 v200, v74, v78 op_sel:[0,0,1]
	v_cvt_pk_fp8_f32 v201, v82, v86
	v_cvt_pk_fp8_f32 v201, v90, v94 op_sel:[0,0,1]
	v_cvt_pk_fp8_f32 v202, v98, v102
	v_cvt_pk_fp8_f32 v202, v106, v110 op_sel:[0,0,1]
	v_cvt_pk_fp8_f32 v203, v114, v118
	v_cvt_pk_fp8_f32 v203, v122, v126 op_sel:[0,0,1]
	global_store_dwordx4 v209, v[200:203], s[26:27] sc1
	v_cvt_pk_fp8_f32 v204, v67, v71
	v_cvt_pk_fp8_f32 v204, v75, v79 op_sel:[0,0,1]
	v_cvt_pk_fp8_f32 v205, v83, v87
	v_cvt_pk_fp8_f32 v205, v91, v95 op_sel:[0,0,1]
	v_cvt_pk_fp8_f32 v206, v99, v103
	v_cvt_pk_fp8_f32 v206, v107, v111 op_sel:[0,0,1]
	v_cvt_pk_fp8_f32 v207, v115, v119
	v_cvt_pk_fp8_f32 v207, v123, v127 op_sel:[0,0,1]
	global_store_dwordx4 v209, v[204:207], s[26:27] offset:2048 sc1
	s_add_i32 s1, s21, 10
	s_and_b32 s1, s1, 15
	s_lshl_b32 s1, s1, 2
	s_add_i32 s1, s1, s20
	s_lshr_b32 s2, s1, 10
	s_and_b32 s4, s1, 0x3ff
	s_lshr_b32 s5, s4, 6
	s_and_b32 s4, s4, 63
	s_lshl_b32 s12, s2, 24
	s_lshl_b32 s13, s5, 20
	s_add_i32 s12, s12, s13
	s_lshl_b32 s13, s4, 7
	s_add_i32 s12, s12, s13
	s_add_u32 s14, s70, s12
	s_addc_u32 s15, s71, 0
	global_load_dwordx4 v[64:67], v208, s[14:15] sc1 nt
	s_add_u32 s18, s14, 0x2000
	s_addc_u32 s19, s15, 0
	global_load_dwordx4 v[68:71], v208, s[18:19] sc1 nt
	s_add_u32 s18, s14, 0x4000
	s_addc_u32 s19, s15, 0
	global_load_dwordx4 v[72:75], v208, s[18:19] sc1 nt
	s_add_u32 s18, s14, 0x6000
	s_addc_u32 s19, s15, 0
	global_load_dwordx4 v[76:79], v208, s[18:19] sc1 nt
	s_add_u32 s18, s14, 0x8000
	s_addc_u32 s19, s15, 0
	global_load_dwordx4 v[80:83], v208, s[18:19] sc1 nt
	s_add_u32 s18, s14, 0xa000
	s_addc_u32 s19, s15, 0
	global_load_dwordx4 v[84:87], v208, s[18:19] sc1 nt
	s_add_u32 s18, s14, 0xc000
	s_addc_u32 s19, s15, 0
	global_load_dwordx4 v[88:91], v208, s[18:19] sc1 nt
	s_add_u32 s18, s14, 0xe000
	s_addc_u32 s19, s15, 0
	global_load_dwordx4 v[92:95], v208, s[18:19] sc1 nt
	s_add_u32 s18, s14, 0x10000
	s_addc_u32 s19, s15, 0
	global_load_dwordx4 v[96:99], v208, s[18:19] sc1 nt
	s_add_u32 s18, s14, 0x12000
	s_addc_u32 s19, s15, 0
	global_load_dwordx4 v[100:103], v208, s[18:19] sc1 nt
	s_add_u32 s18, s14, 0x14000
	s_addc_u32 s19, s15, 0
	global_load_dwordx4 v[104:107], v208, s[18:19] sc1 nt
	s_add_u32 s18, s14, 0x16000
	s_addc_u32 s19, s15, 0
	global_load_dwordx4 v[108:111], v208, s[18:19] sc1 nt
	s_add_u32 s18, s14, 0x18000
	s_addc_u32 s19, s15, 0
	global_load_dwordx4 v[112:115], v208, s[18:19] sc1 nt
	s_add_u32 s18, s14, 0x1a000
	s_addc_u32 s19, s15, 0
	global_load_dwordx4 v[116:119], v208, s[18:19] sc1 nt
	s_add_u32 s18, s14, 0x1c000
	s_addc_u32 s19, s15, 0
	global_load_dwordx4 v[120:123], v208, s[18:19] sc1 nt
	s_add_u32 s18, s14, 0x1e000
	s_addc_u32 s19, s15, 0
	global_load_dwordx4 v[124:127], v208, s[18:19] sc1 nt
	s_waitcnt vmcnt(40)
	s_add_i32 s1, s21, 8
	s_and_b32 s1, s1, 15
	s_lshl_b32 s1, s1, 2
	s_add_i32 s1, s1, s20
	s_lshr_b32 s2, s1, 10
	s_and_b32 s4, s1, 0x3ff
	s_lshr_b32 s5, s4, 6
	s_and_b32 s4, s4, 63
	s_lshl_b32 s12, s2, 22
	s_lshl_b32 s13, s4, 16
	s_add_i32 s12, s12, s13
	s_lshl_b32 s13, s5, 7
	s_add_i32 s12, s12, s13
	s_add_u32 s24, s90, s12
	s_addc_u32 s25, s91, 0
	s_add_u32 s24, s24, 0x3b100000
	s_addc_u32 s25, s25, 0
	s_add_u32 s26, s24, 0x1000
	s_addc_u32 s27, s25, 0
	v_pk_mul_f32 v[128:129], v[128:129], s[16:17] op_sel_hi:[1,0]
	v_pk_mul_f32 v[130:131], v[130:131], s[16:17] op_sel_hi:[1,0]
	v_pk_mul_f32 v[132:133], v[132:133], s[16:17] op_sel_hi:[1,0]
	v_pk_mul_f32 v[134:135], v[134:135], s[16:17] op_sel_hi:[1,0]
	v_pk_mul_f32 v[136:137], v[136:137], s[16:17] op_sel_hi:[1,0]
	v_pk_mul_f32 v[138:139], v[138:139], s[16:17] op_sel_hi:[1,0]
	v_pk_mul_f32 v[140:141], v[140:141], s[16:17] op_sel_hi:[1,0]
	v_pk_mul_f32 v[142:143], v[142:143], s[16:17] op_sel_hi:[1,0]
	v_pk_mul_f32 v[144:145], v[144:145], s[16:17] op_sel_hi:[1,0]
	v_pk_mul_f32 v[146:147], v[146:147], s[16:17] op_sel_hi:[1,0]
	v_pk_mul_f32 v[148:149], v[148:149], s[16:17] op_sel_hi:[1,0]
	v_pk_mul_f32 v[150:151], v[150:151], s[16:17] op_sel_hi:[1,0]
	v_pk_mul_f32 v[152:153], v[152:153], s[16:17] op_sel_hi:[1,0]
	v_pk_mul_f32 v[154:155], v[154:155], s[16:17] op_sel_hi:[1,0]
	v_pk_mul_f32 v[156:157], v[156:157], s[16:17] op_sel_hi:[1,0]
	v_pk_mul_f32 v[158:159], v[158:159], s[16:17] op_sel_hi:[1,0]
	v_pk_mul_f32 v[160:161], v[160:161], s[16:17] op_sel_hi:[1,0]
	v_pk_mul_f32 v[162:163], v[162:163], s[16:17] op_sel_hi:[1,0]
	v_pk_mul_f32 v[164:165], v[164:165], s[16:17] op_sel_hi:[1,0]
	v_pk_mul_f32 v[166:167], v[166:167], s[16:17] op_sel_hi:[1,0]
	v_pk_mul_f32 v[168:169], v[168:169], s[16:17] op_sel_hi:[1,0]
	v_pk_mul_f32 v[170:171], v[170:171], s[16:17] op_sel_hi:[1,0]
	v_pk_mul_f32 v[172:173], v[172:173], s[16:17] op_sel_hi:[1,0]
	v_pk_mul_f32 v[174:175], v[174:175], s[16:17] op_sel_hi:[1,0]
	v_pk_mul_f32 v[176:177], v[176:177], s[16:17] op_sel_hi:[1,0]
	v_pk_mul_f32 v[178:179], v[178:179], s[16:17] op_sel_hi:[1,0]
	v_pk_mul_f32 v[180:181], v[180:181], s[16:17] op_sel_hi:[1,0]
	v_pk_mul_f32 v[182:183], v[182:183], s[16:17] op_sel_hi:[1,0]
	v_pk_mul_f32 v[184:185], v[184:185], s[16:17] op_sel_hi:[1,0]
	v_pk_mul_f32 v[186:187], v[186:187], s[16:17] op_sel_hi:[1,0]
	v_pk_mul_f32 v[188:189], v[188:189], s[16:17] op_sel_hi:[1,0]
	v_pk_mul_f32 v[190:191], v[190:191], s[16:17] op_sel_hi:[1,0]
	v_cvt_pk_fp8_f32 v192, v128, v132
	v_cvt_pk_fp8_f32 v192, v136, v140 op_sel:[0,0,1]
	v_cvt_pk_fp8_f32 v193, v144, v148
	v_cvt_pk_fp8_f32 v193, v152, v156 op_sel:[0,0,1]
	v_cvt_pk_fp8_f32 v194, v160, v164
	v_cvt_pk_fp8_f32 v194, v168, v172 op_sel:[0,0,1]
	v_cvt_pk_fp8_f32 v195, v176, v180
	v_cvt_pk_fp8_f32 v195, v184, v188 op_sel:[0,0,1]
	global_store_dwordx4 v209, v[192:195], s[24:25] sc1
	v_cvt_pk_fp8_f32 v196, v129, v133
	v_cvt_pk_fp8_f32 v196, v137, v141 op_sel:[0,0,1]
	v_cvt_pk_fp8_f32 v197, v145, v149
	v_cvt_pk_fp8_f32 v197, v153, v157 op_sel:[0,0,1]
	v_cvt_pk_fp8_f32 v198, v161, v165
	v_cvt_pk_fp8_f32 v198, v169, v173 op_sel:[0,0,1]
	v_cvt_pk_fp8_f32 v199, v177, v181
	v_cvt_pk_fp8_f32 v199, v185, v189 op_sel:[0,0,1]
	global_store_dwordx4 v209, v[196:199], s[24:25] offset:2048 sc1
	v_cvt_pk_fp8_f32 v200, v130, v134
	v_cvt_pk_fp8_f32 v200, v138, v142 op_sel:[0,0,1]
	v_cvt_pk_fp8_f32 v201, v146, v150
	v_cvt_pk_fp8_f32 v201, v154, v158 op_sel:[0,0,1]
	v_cvt_pk_fp8_f32 v202, v162, v166
	v_cvt_pk_fp8_f32 v202, v170, v174 op_sel:[0,0,1]
	v_cvt_pk_fp8_f32 v203, v178, v182
	v_cvt_pk_fp8_f32 v203, v186, v190 op_sel:[0,0,1]
	global_store_dwordx4 v209, v[200:203], s[26:27] sc1
	v_cvt_pk_fp8_f32 v204, v131, v135
	v_cvt_pk_fp8_f32 v204, v139, v143 op_sel:[0,0,1]
	v_cvt_pk_fp8_f32 v205, v147, v151
	v_cvt_pk_fp8_f32 v205, v155, v159 op_sel:[0,0,1]
	v_cvt_pk_fp8_f32 v206, v163, v167
	v_cvt_pk_fp8_f32 v206, v171, v175 op_sel:[0,0,1]
	v_cvt_pk_fp8_f32 v207, v179, v183
	v_cvt_pk_fp8_f32 v207, v187, v191 op_sel:[0,0,1]
	global_store_dwordx4 v209, v[204:207], s[26:27] offset:2048 sc1
	s_add_i32 s1, s21, 11
	s_and_b32 s1, s1, 15
	s_lshl_b32 s1, s1, 2
	s_add_i32 s1, s1, s20
	s_lshr_b32 s2, s1, 10
	s_and_b32 s4, s1, 0x3ff
	s_lshr_b32 s5, s4, 6
	s_and_b32 s4, s4, 63
	s_lshl_b32 s12, s2, 24
	s_lshl_b32 s13, s5, 20
	s_add_i32 s12, s12, s13
	s_lshl_b32 s13, s4, 7
	s_add_i32 s12, s12, s13
	s_add_u32 s14, s70, s12
	s_addc_u32 s15, s71, 0
	global_load_dwordx4 v[128:131], v208, s[14:15] sc1 nt
	s_add_u32 s18, s14, 0x2000
	s_addc_u32 s19, s15, 0
	global_load_dwordx4 v[132:135], v208, s[18:19] sc1 nt
	s_add_u32 s18, s14, 0x4000
	s_addc_u32 s19, s15, 0
	global_load_dwordx4 v[136:139], v208, s[18:19] sc1 nt
	s_add_u32 s18, s14, 0x6000
	s_addc_u32 s19, s15, 0
	global_load_dwordx4 v[140:143], v208, s[18:19] sc1 nt
	s_add_u32 s18, s14, 0x8000
	s_addc_u32 s19, s15, 0
	global_load_dwordx4 v[144:147], v208, s[18:19] sc1 nt
	s_add_u32 s18, s14, 0xa000
	s_addc_u32 s19, s15, 0
	global_load_dwordx4 v[148:151], v208, s[18:19] sc1 nt
	s_add_u32 s18, s14, 0xc000
	s_addc_u32 s19, s15, 0
	global_load_dwordx4 v[152:155], v208, s[18:19] sc1 nt
	s_add_u32 s18, s14, 0xe000
	s_addc_u32 s19, s15, 0
	global_load_dwordx4 v[156:159], v208, s[18:19] sc1 nt
	s_add_u32 s18, s14, 0x10000
	s_addc_u32 s19, s15, 0
	global_load_dwordx4 v[160:163], v208, s[18:19] sc1 nt
	s_add_u32 s18, s14, 0x12000
	s_addc_u32 s19, s15, 0
	global_load_dwordx4 v[164:167], v208, s[18:19] sc1 nt
	s_add_u32 s18, s14, 0x14000
	s_addc_u32 s19, s15, 0
	global_load_dwordx4 v[168:171], v208, s[18:19] sc1 nt
	s_add_u32 s18, s14, 0x16000
	s_addc_u32 s19, s15, 0
	global_load_dwordx4 v[172:175], v208, s[18:19] sc1 nt
	s_add_u32 s18, s14, 0x18000
	s_addc_u32 s19, s15, 0
	global_load_dwordx4 v[176:179], v208, s[18:19] sc1 nt
	s_add_u32 s18, s14, 0x1a000
	s_addc_u32 s19, s15, 0
	global_load_dwordx4 v[180:183], v208, s[18:19] sc1 nt
	s_add_u32 s18, s14, 0x1c000
	s_addc_u32 s19, s15, 0
	global_load_dwordx4 v[184:187], v208, s[18:19] sc1 nt
	s_add_u32 s18, s14, 0x1e000
	s_addc_u32 s19, s15, 0
	global_load_dwordx4 v[188:191], v208, s[18:19] sc1 nt
	s_waitcnt vmcnt(40)
	s_add_i32 s1, s21, 9
	s_and_b32 s1, s1, 15
	s_lshl_b32 s1, s1, 2
	s_add_i32 s1, s1, s20
	s_lshr_b32 s2, s1, 10
	s_and_b32 s4, s1, 0x3ff
	s_lshr_b32 s5, s4, 6
	s_and_b32 s4, s4, 63
	s_lshl_b32 s12, s2, 22
	s_lshl_b32 s13, s4, 16
	s_add_i32 s12, s12, s13
	s_lshl_b32 s13, s5, 7
	s_add_i32 s12, s12, s13
	s_add_u32 s24, s90, s12
	s_addc_u32 s25, s91, 0
	s_add_u32 s24, s24, 0x3b100000
	s_addc_u32 s25, s25, 0
	s_add_u32 s26, s24, 0x1000
	s_addc_u32 s27, s25, 0
	v_pk_mul_f32 v[0:1], v[0:1], s[16:17] op_sel_hi:[1,0]
	v_pk_mul_f32 v[2:3], v[2:3], s[16:17] op_sel_hi:[1,0]
	v_pk_mul_f32 v[4:5], v[4:5], s[16:17] op_sel_hi:[1,0]
	v_pk_mul_f32 v[6:7], v[6:7], s[16:17] op_sel_hi:[1,0]
	v_pk_mul_f32 v[8:9], v[8:9], s[16:17] op_sel_hi:[1,0]
	v_pk_mul_f32 v[10:11], v[10:11], s[16:17] op_sel_hi:[1,0]
	v_pk_mul_f32 v[12:13], v[12:13], s[16:17] op_sel_hi:[1,0]
	v_pk_mul_f32 v[14:15], v[14:15], s[16:17] op_sel_hi:[1,0]
	v_pk_mul_f32 v[16:17], v[16:17], s[16:17] op_sel_hi:[1,0]
	v_pk_mul_f32 v[18:19], v[18:19], s[16:17] op_sel_hi:[1,0]
	v_pk_mul_f32 v[20:21], v[20:21], s[16:17] op_sel_hi:[1,0]
	v_pk_mul_f32 v[22:23], v[22:23], s[16:17] op_sel_hi:[1,0]
	v_pk_mul_f32 v[24:25], v[24:25], s[16:17] op_sel_hi:[1,0]
	v_pk_mul_f32 v[26:27], v[26:27], s[16:17] op_sel_hi:[1,0]
	v_pk_mul_f32 v[28:29], v[28:29], s[16:17] op_sel_hi:[1,0]
	v_pk_mul_f32 v[30:31], v[30:31], s[16:17] op_sel_hi:[1,0]
	v_pk_mul_f32 v[32:33], v[32:33], s[16:17] op_sel_hi:[1,0]
	v_pk_mul_f32 v[34:35], v[34:35], s[16:17] op_sel_hi:[1,0]
	v_pk_mul_f32 v[36:37], v[36:37], s[16:17] op_sel_hi:[1,0]
	v_pk_mul_f32 v[38:39], v[38:39], s[16:17] op_sel_hi:[1,0]
	v_pk_mul_f32 v[40:41], v[40:41], s[16:17] op_sel_hi:[1,0]
	v_pk_mul_f32 v[42:43], v[42:43], s[16:17] op_sel_hi:[1,0]
	v_pk_mul_f32 v[44:45], v[44:45], s[16:17] op_sel_hi:[1,0]
	v_pk_mul_f32 v[46:47], v[46:47], s[16:17] op_sel_hi:[1,0]
	v_pk_mul_f32 v[48:49], v[48:49], s[16:17] op_sel_hi:[1,0]
	v_pk_mul_f32 v[50:51], v[50:51], s[16:17] op_sel_hi:[1,0]
	v_pk_mul_f32 v[52:53], v[52:53], s[16:17] op_sel_hi:[1,0]
	v_pk_mul_f32 v[54:55], v[54:55], s[16:17] op_sel_hi:[1,0]
	v_pk_mul_f32 v[56:57], v[56:57], s[16:17] op_sel_hi:[1,0]
	v_pk_mul_f32 v[58:59], v[58:59], s[16:17] op_sel_hi:[1,0]
	v_pk_mul_f32 v[60:61], v[60:61], s[16:17] op_sel_hi:[1,0]
	v_pk_mul_f32 v[62:63], v[62:63], s[16:17] op_sel_hi:[1,0]
	v_cvt_pk_fp8_f32 v192, v0, v4
	v_cvt_pk_fp8_f32 v192, v8, v12 op_sel:[0,0,1]
	v_cvt_pk_fp8_f32 v193, v16, v20
	v_cvt_pk_fp8_f32 v193, v24, v28 op_sel:[0,0,1]
	v_cvt_pk_fp8_f32 v194, v32, v36
	v_cvt_pk_fp8_f32 v194, v40, v44 op_sel:[0,0,1]
	v_cvt_pk_fp8_f32 v195, v48, v52
	v_cvt_pk_fp8_f32 v195, v56, v60 op_sel:[0,0,1]
	global_store_dwordx4 v209, v[192:195], s[24:25] sc1
	v_cvt_pk_fp8_f32 v196, v1, v5
	v_cvt_pk_fp8_f32 v196, v9, v13 op_sel:[0,0,1]
	v_cvt_pk_fp8_f32 v197, v17, v21
	v_cvt_pk_fp8_f32 v197, v25, v29 op_sel:[0,0,1]
	v_cvt_pk_fp8_f32 v198, v33, v37
	v_cvt_pk_fp8_f32 v198, v41, v45 op_sel:[0,0,1]
	v_cvt_pk_fp8_f32 v199, v49, v53
	v_cvt_pk_fp8_f32 v199, v57, v61 op_sel:[0,0,1]
	global_store_dwordx4 v209, v[196:199], s[24:25] offset:2048 sc1
	v_cvt_pk_fp8_f32 v200, v2, v6
	v_cvt_pk_fp8_f32 v200, v10, v14 op_sel:[0,0,1]
	v_cvt_pk_fp8_f32 v201, v18, v22
	v_cvt_pk_fp8_f32 v201, v26, v30 op_sel:[0,0,1]
	v_cvt_pk_fp8_f32 v202, v34, v38
	v_cvt_pk_fp8_f32 v202, v42, v46 op_sel:[0,0,1]
	v_cvt_pk_fp8_f32 v203, v50, v54
	v_cvt_pk_fp8_f32 v203, v58, v62 op_sel:[0,0,1]
	global_store_dwordx4 v209, v[200:203], s[26:27] sc1
	v_cvt_pk_fp8_f32 v204, v3, v7
	v_cvt_pk_fp8_f32 v204, v11, v15 op_sel:[0,0,1]
	v_cvt_pk_fp8_f32 v205, v19, v23
	v_cvt_pk_fp8_f32 v205, v27, v31 op_sel:[0,0,1]
	v_cvt_pk_fp8_f32 v206, v35, v39
	v_cvt_pk_fp8_f32 v206, v43, v47 op_sel:[0,0,1]
	v_cvt_pk_fp8_f32 v207, v51, v55
	v_cvt_pk_fp8_f32 v207, v59, v63 op_sel:[0,0,1]
	global_store_dwordx4 v209, v[204:207], s[26:27] offset:2048 sc1
	s_add_i32 s1, s21, 12
	s_and_b32 s1, s1, 15
	s_lshl_b32 s1, s1, 2
	s_add_i32 s1, s1, s20
	s_lshr_b32 s2, s1, 10
	s_and_b32 s4, s1, 0x3ff
	s_lshr_b32 s5, s4, 6
	s_and_b32 s4, s4, 63
	s_lshl_b32 s12, s2, 24
	s_lshl_b32 s13, s5, 20
	s_add_i32 s12, s12, s13
	s_lshl_b32 s13, s4, 7
	s_add_i32 s12, s12, s13
	s_add_u32 s14, s70, s12
	s_addc_u32 s15, s71, 0
	global_load_dwordx4 v[0:3], v208, s[14:15] sc1 nt
	s_add_u32 s18, s14, 0x2000
	s_addc_u32 s19, s15, 0
	global_load_dwordx4 v[4:7], v208, s[18:19] sc1 nt
	s_add_u32 s18, s14, 0x4000
	s_addc_u32 s19, s15, 0
	global_load_dwordx4 v[8:11], v208, s[18:19] sc1 nt
	s_add_u32 s18, s14, 0x6000
	s_addc_u32 s19, s15, 0
	global_load_dwordx4 v[12:15], v208, s[18:19] sc1 nt
	s_add_u32 s18, s14, 0x8000
	s_addc_u32 s19, s15, 0
	global_load_dwordx4 v[16:19], v208, s[18:19] sc1 nt
	s_add_u32 s18, s14, 0xa000
	s_addc_u32 s19, s15, 0
	global_load_dwordx4 v[20:23], v208, s[18:19] sc1 nt
	s_add_u32 s18, s14, 0xc000
	s_addc_u32 s19, s15, 0
	global_load_dwordx4 v[24:27], v208, s[18:19] sc1 nt
	s_add_u32 s18, s14, 0xe000
	s_addc_u32 s19, s15, 0
	global_load_dwordx4 v[28:31], v208, s[18:19] sc1 nt
	s_add_u32 s18, s14, 0x10000
	s_addc_u32 s19, s15, 0
	global_load_dwordx4 v[32:35], v208, s[18:19] sc1 nt
	s_add_u32 s18, s14, 0x12000
	s_addc_u32 s19, s15, 0
	global_load_dwordx4 v[36:39], v208, s[18:19] sc1 nt
	s_add_u32 s18, s14, 0x14000
	s_addc_u32 s19, s15, 0
	global_load_dwordx4 v[40:43], v208, s[18:19] sc1 nt
	s_add_u32 s18, s14, 0x16000
	s_addc_u32 s19, s15, 0
	global_load_dwordx4 v[44:47], v208, s[18:19] sc1 nt
	s_add_u32 s18, s14, 0x18000
	s_addc_u32 s19, s15, 0
	global_load_dwordx4 v[48:51], v208, s[18:19] sc1 nt
	s_add_u32 s18, s14, 0x1a000
	s_addc_u32 s19, s15, 0
	global_load_dwordx4 v[52:55], v208, s[18:19] sc1 nt
	s_add_u32 s18, s14, 0x1c000
	s_addc_u32 s19, s15, 0
	global_load_dwordx4 v[56:59], v208, s[18:19] sc1 nt
	s_add_u32 s18, s14, 0x1e000
	s_addc_u32 s19, s15, 0
	global_load_dwordx4 v[60:63], v208, s[18:19] sc1 nt
	s_waitcnt vmcnt(40)
	s_add_i32 s1, s21, 10
	s_and_b32 s1, s1, 15
	s_lshl_b32 s1, s1, 2
	s_add_i32 s1, s1, s20
	s_lshr_b32 s2, s1, 10
	s_and_b32 s4, s1, 0x3ff
	s_lshr_b32 s5, s4, 6
	s_and_b32 s4, s4, 63
	s_lshl_b32 s12, s2, 22
	s_lshl_b32 s13, s4, 16
	s_add_i32 s12, s12, s13
	s_lshl_b32 s13, s5, 7
	s_add_i32 s12, s12, s13
	s_add_u32 s24, s90, s12
	s_addc_u32 s25, s91, 0
	s_add_u32 s24, s24, 0x3b100000
	s_addc_u32 s25, s25, 0
	s_add_u32 s26, s24, 0x1000
	s_addc_u32 s27, s25, 0
	v_pk_mul_f32 v[64:65], v[64:65], s[16:17] op_sel_hi:[1,0]
	v_pk_mul_f32 v[66:67], v[66:67], s[16:17] op_sel_hi:[1,0]
	v_pk_mul_f32 v[68:69], v[68:69], s[16:17] op_sel_hi:[1,0]
	v_pk_mul_f32 v[70:71], v[70:71], s[16:17] op_sel_hi:[1,0]
	v_pk_mul_f32 v[72:73], v[72:73], s[16:17] op_sel_hi:[1,0]
	v_pk_mul_f32 v[74:75], v[74:75], s[16:17] op_sel_hi:[1,0]
	v_pk_mul_f32 v[76:77], v[76:77], s[16:17] op_sel_hi:[1,0]
	v_pk_mul_f32 v[78:79], v[78:79], s[16:17] op_sel_hi:[1,0]
	v_pk_mul_f32 v[80:81], v[80:81], s[16:17] op_sel_hi:[1,0]
	v_pk_mul_f32 v[82:83], v[82:83], s[16:17] op_sel_hi:[1,0]
	v_pk_mul_f32 v[84:85], v[84:85], s[16:17] op_sel_hi:[1,0]
	v_pk_mul_f32 v[86:87], v[86:87], s[16:17] op_sel_hi:[1,0]
	v_pk_mul_f32 v[88:89], v[88:89], s[16:17] op_sel_hi:[1,0]
	v_pk_mul_f32 v[90:91], v[90:91], s[16:17] op_sel_hi:[1,0]
	v_pk_mul_f32 v[92:93], v[92:93], s[16:17] op_sel_hi:[1,0]
	v_pk_mul_f32 v[94:95], v[94:95], s[16:17] op_sel_hi:[1,0]
	v_pk_mul_f32 v[96:97], v[96:97], s[16:17] op_sel_hi:[1,0]
	v_pk_mul_f32 v[98:99], v[98:99], s[16:17] op_sel_hi:[1,0]
	v_pk_mul_f32 v[100:101], v[100:101], s[16:17] op_sel_hi:[1,0]
	v_pk_mul_f32 v[102:103], v[102:103], s[16:17] op_sel_hi:[1,0]
	v_pk_mul_f32 v[104:105], v[104:105], s[16:17] op_sel_hi:[1,0]
	v_pk_mul_f32 v[106:107], v[106:107], s[16:17] op_sel_hi:[1,0]
	v_pk_mul_f32 v[108:109], v[108:109], s[16:17] op_sel_hi:[1,0]
	v_pk_mul_f32 v[110:111], v[110:111], s[16:17] op_sel_hi:[1,0]
	v_pk_mul_f32 v[112:113], v[112:113], s[16:17] op_sel_hi:[1,0]
	v_pk_mul_f32 v[114:115], v[114:115], s[16:17] op_sel_hi:[1,0]
	v_pk_mul_f32 v[116:117], v[116:117], s[16:17] op_sel_hi:[1,0]
	v_pk_mul_f32 v[118:119], v[118:119], s[16:17] op_sel_hi:[1,0]
	v_pk_mul_f32 v[120:121], v[120:121], s[16:17] op_sel_hi:[1,0]
	v_pk_mul_f32 v[122:123], v[122:123], s[16:17] op_sel_hi:[1,0]
	v_pk_mul_f32 v[124:125], v[124:125], s[16:17] op_sel_hi:[1,0]
	v_pk_mul_f32 v[126:127], v[126:127], s[16:17] op_sel_hi:[1,0]
	v_cvt_pk_fp8_f32 v192, v64, v68
	v_cvt_pk_fp8_f32 v192, v72, v76 op_sel:[0,0,1]
	v_cvt_pk_fp8_f32 v193, v80, v84
	v_cvt_pk_fp8_f32 v193, v88, v92 op_sel:[0,0,1]
	v_cvt_pk_fp8_f32 v194, v96, v100
	v_cvt_pk_fp8_f32 v194, v104, v108 op_sel:[0,0,1]
	v_cvt_pk_fp8_f32 v195, v112, v116
	v_cvt_pk_fp8_f32 v195, v120, v124 op_sel:[0,0,1]
	global_store_dwordx4 v209, v[192:195], s[24:25] sc1
	v_cvt_pk_fp8_f32 v196, v65, v69
	v_cvt_pk_fp8_f32 v196, v73, v77 op_sel:[0,0,1]
	v_cvt_pk_fp8_f32 v197, v81, v85
	v_cvt_pk_fp8_f32 v197, v89, v93 op_sel:[0,0,1]
	v_cvt_pk_fp8_f32 v198, v97, v101
	v_cvt_pk_fp8_f32 v198, v105, v109 op_sel:[0,0,1]
	v_cvt_pk_fp8_f32 v199, v113, v117
	v_cvt_pk_fp8_f32 v199, v121, v125 op_sel:[0,0,1]
	global_store_dwordx4 v209, v[196:199], s[24:25] offset:2048 sc1
	v_cvt_pk_fp8_f32 v200, v66, v70
	v_cvt_pk_fp8_f32 v200, v74, v78 op_sel:[0,0,1]
	v_cvt_pk_fp8_f32 v201, v82, v86
	v_cvt_pk_fp8_f32 v201, v90, v94 op_sel:[0,0,1]
	v_cvt_pk_fp8_f32 v202, v98, v102
	v_cvt_pk_fp8_f32 v202, v106, v110 op_sel:[0,0,1]
	v_cvt_pk_fp8_f32 v203, v114, v118
	v_cvt_pk_fp8_f32 v203, v122, v126 op_sel:[0,0,1]
	global_store_dwordx4 v209, v[200:203], s[26:27] sc1
	v_cvt_pk_fp8_f32 v204, v67, v71
	v_cvt_pk_fp8_f32 v204, v75, v79 op_sel:[0,0,1]
	v_cvt_pk_fp8_f32 v205, v83, v87
	v_cvt_pk_fp8_f32 v205, v91, v95 op_sel:[0,0,1]
	v_cvt_pk_fp8_f32 v206, v99, v103
	v_cvt_pk_fp8_f32 v206, v107, v111 op_sel:[0,0,1]
	v_cvt_pk_fp8_f32 v207, v115, v119
	v_cvt_pk_fp8_f32 v207, v123, v127 op_sel:[0,0,1]
	global_store_dwordx4 v209, v[204:207], s[26:27] offset:2048 sc1
	s_add_i32 s1, s21, 13
	s_and_b32 s1, s1, 15
	s_lshl_b32 s1, s1, 2
	s_add_i32 s1, s1, s20
	s_lshr_b32 s2, s1, 10
	s_and_b32 s4, s1, 0x3ff
	s_lshr_b32 s5, s4, 6
	s_and_b32 s4, s4, 63
	s_lshl_b32 s12, s2, 24
	s_lshl_b32 s13, s5, 20
	s_add_i32 s12, s12, s13
	s_lshl_b32 s13, s4, 7
	s_add_i32 s12, s12, s13
	s_add_u32 s14, s70, s12
	s_addc_u32 s15, s71, 0
	global_load_dwordx4 v[64:67], v208, s[14:15] sc1 nt
	s_add_u32 s18, s14, 0x2000
	s_addc_u32 s19, s15, 0
	global_load_dwordx4 v[68:71], v208, s[18:19] sc1 nt
	s_add_u32 s18, s14, 0x4000
	s_addc_u32 s19, s15, 0
	global_load_dwordx4 v[72:75], v208, s[18:19] sc1 nt
	s_add_u32 s18, s14, 0x6000
	s_addc_u32 s19, s15, 0
	global_load_dwordx4 v[76:79], v208, s[18:19] sc1 nt
	s_add_u32 s18, s14, 0x8000
	s_addc_u32 s19, s15, 0
	global_load_dwordx4 v[80:83], v208, s[18:19] sc1 nt
	s_add_u32 s18, s14, 0xa000
	s_addc_u32 s19, s15, 0
	global_load_dwordx4 v[84:87], v208, s[18:19] sc1 nt
	s_add_u32 s18, s14, 0xc000
	s_addc_u32 s19, s15, 0
	global_load_dwordx4 v[88:91], v208, s[18:19] sc1 nt
	s_add_u32 s18, s14, 0xe000
	s_addc_u32 s19, s15, 0
	global_load_dwordx4 v[92:95], v208, s[18:19] sc1 nt
	s_add_u32 s18, s14, 0x10000
	s_addc_u32 s19, s15, 0
	global_load_dwordx4 v[96:99], v208, s[18:19] sc1 nt
	s_add_u32 s18, s14, 0x12000
	s_addc_u32 s19, s15, 0
	global_load_dwordx4 v[100:103], v208, s[18:19] sc1 nt
	s_add_u32 s18, s14, 0x14000
	s_addc_u32 s19, s15, 0
	global_load_dwordx4 v[104:107], v208, s[18:19] sc1 nt
	s_add_u32 s18, s14, 0x16000
	s_addc_u32 s19, s15, 0
	global_load_dwordx4 v[108:111], v208, s[18:19] sc1 nt
	s_add_u32 s18, s14, 0x18000
	s_addc_u32 s19, s15, 0
	global_load_dwordx4 v[112:115], v208, s[18:19] sc1 nt
	s_add_u32 s18, s14, 0x1a000
	s_addc_u32 s19, s15, 0
	global_load_dwordx4 v[116:119], v208, s[18:19] sc1 nt
	s_add_u32 s18, s14, 0x1c000
	s_addc_u32 s19, s15, 0
	global_load_dwordx4 v[120:123], v208, s[18:19] sc1 nt
	s_add_u32 s18, s14, 0x1e000
	s_addc_u32 s19, s15, 0
	global_load_dwordx4 v[124:127], v208, s[18:19] sc1 nt
	s_waitcnt vmcnt(40)
	s_add_i32 s1, s21, 11
	s_and_b32 s1, s1, 15
	s_lshl_b32 s1, s1, 2
	s_add_i32 s1, s1, s20
	s_lshr_b32 s2, s1, 10
	s_and_b32 s4, s1, 0x3ff
	s_lshr_b32 s5, s4, 6
	s_and_b32 s4, s4, 63
	s_lshl_b32 s12, s2, 22
	s_lshl_b32 s13, s4, 16
	s_add_i32 s12, s12, s13
	s_lshl_b32 s13, s5, 7
	s_add_i32 s12, s12, s13
	s_add_u32 s24, s90, s12
	s_addc_u32 s25, s91, 0
	s_add_u32 s24, s24, 0x3b100000
	s_addc_u32 s25, s25, 0
	s_add_u32 s26, s24, 0x1000
	s_addc_u32 s27, s25, 0
	v_pk_mul_f32 v[128:129], v[128:129], s[16:17] op_sel_hi:[1,0]
	v_pk_mul_f32 v[130:131], v[130:131], s[16:17] op_sel_hi:[1,0]
	v_pk_mul_f32 v[132:133], v[132:133], s[16:17] op_sel_hi:[1,0]
	v_pk_mul_f32 v[134:135], v[134:135], s[16:17] op_sel_hi:[1,0]
	v_pk_mul_f32 v[136:137], v[136:137], s[16:17] op_sel_hi:[1,0]
	v_pk_mul_f32 v[138:139], v[138:139], s[16:17] op_sel_hi:[1,0]
	v_pk_mul_f32 v[140:141], v[140:141], s[16:17] op_sel_hi:[1,0]
	v_pk_mul_f32 v[142:143], v[142:143], s[16:17] op_sel_hi:[1,0]
	v_pk_mul_f32 v[144:145], v[144:145], s[16:17] op_sel_hi:[1,0]
	v_pk_mul_f32 v[146:147], v[146:147], s[16:17] op_sel_hi:[1,0]
	v_pk_mul_f32 v[148:149], v[148:149], s[16:17] op_sel_hi:[1,0]
	v_pk_mul_f32 v[150:151], v[150:151], s[16:17] op_sel_hi:[1,0]
	v_pk_mul_f32 v[152:153], v[152:153], s[16:17] op_sel_hi:[1,0]
	v_pk_mul_f32 v[154:155], v[154:155], s[16:17] op_sel_hi:[1,0]
	v_pk_mul_f32 v[156:157], v[156:157], s[16:17] op_sel_hi:[1,0]
	v_pk_mul_f32 v[158:159], v[158:159], s[16:17] op_sel_hi:[1,0]
	v_pk_mul_f32 v[160:161], v[160:161], s[16:17] op_sel_hi:[1,0]
	v_pk_mul_f32 v[162:163], v[162:163], s[16:17] op_sel_hi:[1,0]
	v_pk_mul_f32 v[164:165], v[164:165], s[16:17] op_sel_hi:[1,0]
	v_pk_mul_f32 v[166:167], v[166:167], s[16:17] op_sel_hi:[1,0]
	v_pk_mul_f32 v[168:169], v[168:169], s[16:17] op_sel_hi:[1,0]
	v_pk_mul_f32 v[170:171], v[170:171], s[16:17] op_sel_hi:[1,0]
	v_pk_mul_f32 v[172:173], v[172:173], s[16:17] op_sel_hi:[1,0]
	v_pk_mul_f32 v[174:175], v[174:175], s[16:17] op_sel_hi:[1,0]
	v_pk_mul_f32 v[176:177], v[176:177], s[16:17] op_sel_hi:[1,0]
	v_pk_mul_f32 v[178:179], v[178:179], s[16:17] op_sel_hi:[1,0]
	v_pk_mul_f32 v[180:181], v[180:181], s[16:17] op_sel_hi:[1,0]
	v_pk_mul_f32 v[182:183], v[182:183], s[16:17] op_sel_hi:[1,0]
	v_pk_mul_f32 v[184:185], v[184:185], s[16:17] op_sel_hi:[1,0]
	v_pk_mul_f32 v[186:187], v[186:187], s[16:17] op_sel_hi:[1,0]
	v_pk_mul_f32 v[188:189], v[188:189], s[16:17] op_sel_hi:[1,0]
	v_pk_mul_f32 v[190:191], v[190:191], s[16:17] op_sel_hi:[1,0]
	v_cvt_pk_fp8_f32 v192, v128, v132
	v_cvt_pk_fp8_f32 v192, v136, v140 op_sel:[0,0,1]
	v_cvt_pk_fp8_f32 v193, v144, v148
	v_cvt_pk_fp8_f32 v193, v152, v156 op_sel:[0,0,1]
	v_cvt_pk_fp8_f32 v194, v160, v164
	v_cvt_pk_fp8_f32 v194, v168, v172 op_sel:[0,0,1]
	v_cvt_pk_fp8_f32 v195, v176, v180
	v_cvt_pk_fp8_f32 v195, v184, v188 op_sel:[0,0,1]
	global_store_dwordx4 v209, v[192:195], s[24:25] sc1
	v_cvt_pk_fp8_f32 v196, v129, v133
	v_cvt_pk_fp8_f32 v196, v137, v141 op_sel:[0,0,1]
	v_cvt_pk_fp8_f32 v197, v145, v149
	v_cvt_pk_fp8_f32 v197, v153, v157 op_sel:[0,0,1]
	v_cvt_pk_fp8_f32 v198, v161, v165
	v_cvt_pk_fp8_f32 v198, v169, v173 op_sel:[0,0,1]
	v_cvt_pk_fp8_f32 v199, v177, v181
	v_cvt_pk_fp8_f32 v199, v185, v189 op_sel:[0,0,1]
	global_store_dwordx4 v209, v[196:199], s[24:25] offset:2048 sc1
	v_cvt_pk_fp8_f32 v200, v130, v134
	v_cvt_pk_fp8_f32 v200, v138, v142 op_sel:[0,0,1]
	v_cvt_pk_fp8_f32 v201, v146, v150
	v_cvt_pk_fp8_f32 v201, v154, v158 op_sel:[0,0,1]
	v_cvt_pk_fp8_f32 v202, v162, v166
	v_cvt_pk_fp8_f32 v202, v170, v174 op_sel:[0,0,1]
	v_cvt_pk_fp8_f32 v203, v178, v182
	v_cvt_pk_fp8_f32 v203, v186, v190 op_sel:[0,0,1]
	global_store_dwordx4 v209, v[200:203], s[26:27] sc1
	v_cvt_pk_fp8_f32 v204, v131, v135
	v_cvt_pk_fp8_f32 v204, v139, v143 op_sel:[0,0,1]
	v_cvt_pk_fp8_f32 v205, v147, v151
	v_cvt_pk_fp8_f32 v205, v155, v159 op_sel:[0,0,1]
	v_cvt_pk_fp8_f32 v206, v163, v167
	v_cvt_pk_fp8_f32 v206, v171, v175 op_sel:[0,0,1]
	v_cvt_pk_fp8_f32 v207, v179, v183
	v_cvt_pk_fp8_f32 v207, v187, v191 op_sel:[0,0,1]
	global_store_dwordx4 v209, v[204:207], s[26:27] offset:2048 sc1
	s_add_i32 s1, s21, 14
	s_and_b32 s1, s1, 15
	s_lshl_b32 s1, s1, 2
	s_add_i32 s1, s1, s20
	s_lshr_b32 s2, s1, 10
	s_and_b32 s4, s1, 0x3ff
	s_lshr_b32 s5, s4, 6
	s_and_b32 s4, s4, 63
	s_lshl_b32 s12, s2, 24
	s_lshl_b32 s13, s5, 20
	s_add_i32 s12, s12, s13
	s_lshl_b32 s13, s4, 7
	s_add_i32 s12, s12, s13
	s_add_u32 s14, s70, s12
	s_addc_u32 s15, s71, 0
	global_load_dwordx4 v[128:131], v208, s[14:15] sc1 nt
	s_add_u32 s18, s14, 0x2000
	s_addc_u32 s19, s15, 0
	global_load_dwordx4 v[132:135], v208, s[18:19] sc1 nt
	s_add_u32 s18, s14, 0x4000
	s_addc_u32 s19, s15, 0
	global_load_dwordx4 v[136:139], v208, s[18:19] sc1 nt
	s_add_u32 s18, s14, 0x6000
	s_addc_u32 s19, s15, 0
	global_load_dwordx4 v[140:143], v208, s[18:19] sc1 nt
	s_add_u32 s18, s14, 0x8000
	s_addc_u32 s19, s15, 0
	global_load_dwordx4 v[144:147], v208, s[18:19] sc1 nt
	s_add_u32 s18, s14, 0xa000
	s_addc_u32 s19, s15, 0
	global_load_dwordx4 v[148:151], v208, s[18:19] sc1 nt
	s_add_u32 s18, s14, 0xc000
	s_addc_u32 s19, s15, 0
	global_load_dwordx4 v[152:155], v208, s[18:19] sc1 nt
	s_add_u32 s18, s14, 0xe000
	s_addc_u32 s19, s15, 0
	global_load_dwordx4 v[156:159], v208, s[18:19] sc1 nt
	s_add_u32 s18, s14, 0x10000
	s_addc_u32 s19, s15, 0
	global_load_dwordx4 v[160:163], v208, s[18:19] sc1 nt
	s_add_u32 s18, s14, 0x12000
	s_addc_u32 s19, s15, 0
	global_load_dwordx4 v[164:167], v208, s[18:19] sc1 nt
	s_add_u32 s18, s14, 0x14000
	s_addc_u32 s19, s15, 0
	global_load_dwordx4 v[168:171], v208, s[18:19] sc1 nt
	s_add_u32 s18, s14, 0x16000
	s_addc_u32 s19, s15, 0
	global_load_dwordx4 v[172:175], v208, s[18:19] sc1 nt
	s_add_u32 s18, s14, 0x18000
	s_addc_u32 s19, s15, 0
	global_load_dwordx4 v[176:179], v208, s[18:19] sc1 nt
	s_add_u32 s18, s14, 0x1a000
	s_addc_u32 s19, s15, 0
	global_load_dwordx4 v[180:183], v208, s[18:19] sc1 nt
	s_add_u32 s18, s14, 0x1c000
	s_addc_u32 s19, s15, 0
	global_load_dwordx4 v[184:187], v208, s[18:19] sc1 nt
	s_add_u32 s18, s14, 0x1e000
	s_addc_u32 s19, s15, 0
	global_load_dwordx4 v[188:191], v208, s[18:19] sc1 nt
	s_waitcnt vmcnt(40)
	s_add_i32 s1, s21, 12
	s_and_b32 s1, s1, 15
	s_lshl_b32 s1, s1, 2
	s_add_i32 s1, s1, s20
	s_lshr_b32 s2, s1, 10
	s_and_b32 s4, s1, 0x3ff
	s_lshr_b32 s5, s4, 6
	s_and_b32 s4, s4, 63
	s_lshl_b32 s12, s2, 22
	s_lshl_b32 s13, s4, 16
	s_add_i32 s12, s12, s13
	s_lshl_b32 s13, s5, 7
	s_add_i32 s12, s12, s13
	s_add_u32 s24, s90, s12
	s_addc_u32 s25, s91, 0
	s_add_u32 s24, s24, 0x3b100000
	s_addc_u32 s25, s25, 0
	s_add_u32 s26, s24, 0x1000
	s_addc_u32 s27, s25, 0
	v_pk_mul_f32 v[0:1], v[0:1], s[16:17] op_sel_hi:[1,0]
	v_pk_mul_f32 v[2:3], v[2:3], s[16:17] op_sel_hi:[1,0]
	v_pk_mul_f32 v[4:5], v[4:5], s[16:17] op_sel_hi:[1,0]
	v_pk_mul_f32 v[6:7], v[6:7], s[16:17] op_sel_hi:[1,0]
	v_pk_mul_f32 v[8:9], v[8:9], s[16:17] op_sel_hi:[1,0]
	v_pk_mul_f32 v[10:11], v[10:11], s[16:17] op_sel_hi:[1,0]
	v_pk_mul_f32 v[12:13], v[12:13], s[16:17] op_sel_hi:[1,0]
	v_pk_mul_f32 v[14:15], v[14:15], s[16:17] op_sel_hi:[1,0]
	v_pk_mul_f32 v[16:17], v[16:17], s[16:17] op_sel_hi:[1,0]
	v_pk_mul_f32 v[18:19], v[18:19], s[16:17] op_sel_hi:[1,0]
	v_pk_mul_f32 v[20:21], v[20:21], s[16:17] op_sel_hi:[1,0]
	v_pk_mul_f32 v[22:23], v[22:23], s[16:17] op_sel_hi:[1,0]
	v_pk_mul_f32 v[24:25], v[24:25], s[16:17] op_sel_hi:[1,0]
	v_pk_mul_f32 v[26:27], v[26:27], s[16:17] op_sel_hi:[1,0]
	v_pk_mul_f32 v[28:29], v[28:29], s[16:17] op_sel_hi:[1,0]
	v_pk_mul_f32 v[30:31], v[30:31], s[16:17] op_sel_hi:[1,0]
	v_pk_mul_f32 v[32:33], v[32:33], s[16:17] op_sel_hi:[1,0]
	v_pk_mul_f32 v[34:35], v[34:35], s[16:17] op_sel_hi:[1,0]
	v_pk_mul_f32 v[36:37], v[36:37], s[16:17] op_sel_hi:[1,0]
	v_pk_mul_f32 v[38:39], v[38:39], s[16:17] op_sel_hi:[1,0]
	v_pk_mul_f32 v[40:41], v[40:41], s[16:17] op_sel_hi:[1,0]
	v_pk_mul_f32 v[42:43], v[42:43], s[16:17] op_sel_hi:[1,0]
	v_pk_mul_f32 v[44:45], v[44:45], s[16:17] op_sel_hi:[1,0]
	v_pk_mul_f32 v[46:47], v[46:47], s[16:17] op_sel_hi:[1,0]
	v_pk_mul_f32 v[48:49], v[48:49], s[16:17] op_sel_hi:[1,0]
	v_pk_mul_f32 v[50:51], v[50:51], s[16:17] op_sel_hi:[1,0]
	v_pk_mul_f32 v[52:53], v[52:53], s[16:17] op_sel_hi:[1,0]
	v_pk_mul_f32 v[54:55], v[54:55], s[16:17] op_sel_hi:[1,0]
	v_pk_mul_f32 v[56:57], v[56:57], s[16:17] op_sel_hi:[1,0]
	v_pk_mul_f32 v[58:59], v[58:59], s[16:17] op_sel_hi:[1,0]
	v_pk_mul_f32 v[60:61], v[60:61], s[16:17] op_sel_hi:[1,0]
	v_pk_mul_f32 v[62:63], v[62:63], s[16:17] op_sel_hi:[1,0]
	v_cvt_pk_fp8_f32 v192, v0, v4
	v_cvt_pk_fp8_f32 v192, v8, v12 op_sel:[0,0,1]
	v_cvt_pk_fp8_f32 v193, v16, v20
	v_cvt_pk_fp8_f32 v193, v24, v28 op_sel:[0,0,1]
	v_cvt_pk_fp8_f32 v194, v32, v36
	v_cvt_pk_fp8_f32 v194, v40, v44 op_sel:[0,0,1]
	v_cvt_pk_fp8_f32 v195, v48, v52
	v_cvt_pk_fp8_f32 v195, v56, v60 op_sel:[0,0,1]
	global_store_dwordx4 v209, v[192:195], s[24:25] sc1
	v_cvt_pk_fp8_f32 v196, v1, v5
	v_cvt_pk_fp8_f32 v196, v9, v13 op_sel:[0,0,1]
	v_cvt_pk_fp8_f32 v197, v17, v21
	v_cvt_pk_fp8_f32 v197, v25, v29 op_sel:[0,0,1]
	v_cvt_pk_fp8_f32 v198, v33, v37
	v_cvt_pk_fp8_f32 v198, v41, v45 op_sel:[0,0,1]
	v_cvt_pk_fp8_f32 v199, v49, v53
	v_cvt_pk_fp8_f32 v199, v57, v61 op_sel:[0,0,1]
	global_store_dwordx4 v209, v[196:199], s[24:25] offset:2048 sc1
	v_cvt_pk_fp8_f32 v200, v2, v6
	v_cvt_pk_fp8_f32 v200, v10, v14 op_sel:[0,0,1]
	v_cvt_pk_fp8_f32 v201, v18, v22
	v_cvt_pk_fp8_f32 v201, v26, v30 op_sel:[0,0,1]
	v_cvt_pk_fp8_f32 v202, v34, v38
	v_cvt_pk_fp8_f32 v202, v42, v46 op_sel:[0,0,1]
	v_cvt_pk_fp8_f32 v203, v50, v54
	v_cvt_pk_fp8_f32 v203, v58, v62 op_sel:[0,0,1]
	global_store_dwordx4 v209, v[200:203], s[26:27] sc1
	v_cvt_pk_fp8_f32 v204, v3, v7
	v_cvt_pk_fp8_f32 v204, v11, v15 op_sel:[0,0,1]
	v_cvt_pk_fp8_f32 v205, v19, v23
	v_cvt_pk_fp8_f32 v205, v27, v31 op_sel:[0,0,1]
	v_cvt_pk_fp8_f32 v206, v35, v39
	v_cvt_pk_fp8_f32 v206, v43, v47 op_sel:[0,0,1]
	v_cvt_pk_fp8_f32 v207, v51, v55
	v_cvt_pk_fp8_f32 v207, v59, v63 op_sel:[0,0,1]
	global_store_dwordx4 v209, v[204:207], s[26:27] offset:2048 sc1
	s_add_i32 s1, s21, 15
	s_and_b32 s1, s1, 15
	s_lshl_b32 s1, s1, 2
	s_add_i32 s1, s1, s20
	s_lshr_b32 s2, s1, 10
	s_and_b32 s4, s1, 0x3ff
	s_lshr_b32 s5, s4, 6
	s_and_b32 s4, s4, 63
	s_lshl_b32 s12, s2, 24
	s_lshl_b32 s13, s5, 20
	s_add_i32 s12, s12, s13
	s_lshl_b32 s13, s4, 7
	s_add_i32 s12, s12, s13
	s_add_u32 s14, s70, s12
	s_addc_u32 s15, s71, 0
	global_load_dwordx4 v[0:3], v208, s[14:15] sc1 nt
	s_add_u32 s18, s14, 0x2000
	s_addc_u32 s19, s15, 0
	global_load_dwordx4 v[4:7], v208, s[18:19] sc1 nt
	s_add_u32 s18, s14, 0x4000
	s_addc_u32 s19, s15, 0
	global_load_dwordx4 v[8:11], v208, s[18:19] sc1 nt
	s_add_u32 s18, s14, 0x6000
	s_addc_u32 s19, s15, 0
	global_load_dwordx4 v[12:15], v208, s[18:19] sc1 nt
	s_add_u32 s18, s14, 0x8000
	s_addc_u32 s19, s15, 0
	global_load_dwordx4 v[16:19], v208, s[18:19] sc1 nt
	s_add_u32 s18, s14, 0xa000
	s_addc_u32 s19, s15, 0
	global_load_dwordx4 v[20:23], v208, s[18:19] sc1 nt
	s_add_u32 s18, s14, 0xc000
	s_addc_u32 s19, s15, 0
	global_load_dwordx4 v[24:27], v208, s[18:19] sc1 nt
	s_add_u32 s18, s14, 0xe000
	s_addc_u32 s19, s15, 0
	global_load_dwordx4 v[28:31], v208, s[18:19] sc1 nt
	s_add_u32 s18, s14, 0x10000
	s_addc_u32 s19, s15, 0
	global_load_dwordx4 v[32:35], v208, s[18:19] sc1 nt
	s_add_u32 s18, s14, 0x12000
	s_addc_u32 s19, s15, 0
	global_load_dwordx4 v[36:39], v208, s[18:19] sc1 nt
	s_add_u32 s18, s14, 0x14000
	s_addc_u32 s19, s15, 0
	global_load_dwordx4 v[40:43], v208, s[18:19] sc1 nt
	s_add_u32 s18, s14, 0x16000
	s_addc_u32 s19, s15, 0
	global_load_dwordx4 v[44:47], v208, s[18:19] sc1 nt
	s_add_u32 s18, s14, 0x18000
	s_addc_u32 s19, s15, 0
	global_load_dwordx4 v[48:51], v208, s[18:19] sc1 nt
	s_add_u32 s18, s14, 0x1a000
	s_addc_u32 s19, s15, 0
	global_load_dwordx4 v[52:55], v208, s[18:19] sc1 nt
	s_add_u32 s18, s14, 0x1c000
	s_addc_u32 s19, s15, 0
	global_load_dwordx4 v[56:59], v208, s[18:19] sc1 nt
	s_add_u32 s18, s14, 0x1e000
	s_addc_u32 s19, s15, 0
	global_load_dwordx4 v[60:63], v208, s[18:19] sc1 nt
	s_waitcnt vmcnt(40)
	s_add_i32 s1, s21, 13
	s_and_b32 s1, s1, 15
	s_lshl_b32 s1, s1, 2
	s_add_i32 s1, s1, s20
	s_lshr_b32 s2, s1, 10
	s_and_b32 s4, s1, 0x3ff
	s_lshr_b32 s5, s4, 6
	s_and_b32 s4, s4, 63
	s_lshl_b32 s12, s2, 22
	s_lshl_b32 s13, s4, 16
	s_add_i32 s12, s12, s13
	s_lshl_b32 s13, s5, 7
	s_add_i32 s12, s12, s13
	s_add_u32 s24, s90, s12
	s_addc_u32 s25, s91, 0
	s_add_u32 s24, s24, 0x3b100000
	s_addc_u32 s25, s25, 0
	s_add_u32 s26, s24, 0x1000
	s_addc_u32 s27, s25, 0
	v_pk_mul_f32 v[64:65], v[64:65], s[16:17] op_sel_hi:[1,0]
	v_pk_mul_f32 v[66:67], v[66:67], s[16:17] op_sel_hi:[1,0]
	v_pk_mul_f32 v[68:69], v[68:69], s[16:17] op_sel_hi:[1,0]
	v_pk_mul_f32 v[70:71], v[70:71], s[16:17] op_sel_hi:[1,0]
	v_pk_mul_f32 v[72:73], v[72:73], s[16:17] op_sel_hi:[1,0]
	v_pk_mul_f32 v[74:75], v[74:75], s[16:17] op_sel_hi:[1,0]
	v_pk_mul_f32 v[76:77], v[76:77], s[16:17] op_sel_hi:[1,0]
	v_pk_mul_f32 v[78:79], v[78:79], s[16:17] op_sel_hi:[1,0]
	v_pk_mul_f32 v[80:81], v[80:81], s[16:17] op_sel_hi:[1,0]
	v_pk_mul_f32 v[82:83], v[82:83], s[16:17] op_sel_hi:[1,0]
	v_pk_mul_f32 v[84:85], v[84:85], s[16:17] op_sel_hi:[1,0]
	v_pk_mul_f32 v[86:87], v[86:87], s[16:17] op_sel_hi:[1,0]
	v_pk_mul_f32 v[88:89], v[88:89], s[16:17] op_sel_hi:[1,0]
	v_pk_mul_f32 v[90:91], v[90:91], s[16:17] op_sel_hi:[1,0]
	v_pk_mul_f32 v[92:93], v[92:93], s[16:17] op_sel_hi:[1,0]
	v_pk_mul_f32 v[94:95], v[94:95], s[16:17] op_sel_hi:[1,0]
	v_pk_mul_f32 v[96:97], v[96:97], s[16:17] op_sel_hi:[1,0]
	v_pk_mul_f32 v[98:99], v[98:99], s[16:17] op_sel_hi:[1,0]
	v_pk_mul_f32 v[100:101], v[100:101], s[16:17] op_sel_hi:[1,0]
	v_pk_mul_f32 v[102:103], v[102:103], s[16:17] op_sel_hi:[1,0]
	v_pk_mul_f32 v[104:105], v[104:105], s[16:17] op_sel_hi:[1,0]
	v_pk_mul_f32 v[106:107], v[106:107], s[16:17] op_sel_hi:[1,0]
	v_pk_mul_f32 v[108:109], v[108:109], s[16:17] op_sel_hi:[1,0]
	v_pk_mul_f32 v[110:111], v[110:111], s[16:17] op_sel_hi:[1,0]
	v_pk_mul_f32 v[112:113], v[112:113], s[16:17] op_sel_hi:[1,0]
	v_pk_mul_f32 v[114:115], v[114:115], s[16:17] op_sel_hi:[1,0]
	v_pk_mul_f32 v[116:117], v[116:117], s[16:17] op_sel_hi:[1,0]
	v_pk_mul_f32 v[118:119], v[118:119], s[16:17] op_sel_hi:[1,0]
	v_pk_mul_f32 v[120:121], v[120:121], s[16:17] op_sel_hi:[1,0]
	v_pk_mul_f32 v[122:123], v[122:123], s[16:17] op_sel_hi:[1,0]
	v_pk_mul_f32 v[124:125], v[124:125], s[16:17] op_sel_hi:[1,0]
	v_pk_mul_f32 v[126:127], v[126:127], s[16:17] op_sel_hi:[1,0]
	v_cvt_pk_fp8_f32 v192, v64, v68
	v_cvt_pk_fp8_f32 v192, v72, v76 op_sel:[0,0,1]
	v_cvt_pk_fp8_f32 v193, v80, v84
	v_cvt_pk_fp8_f32 v193, v88, v92 op_sel:[0,0,1]
	v_cvt_pk_fp8_f32 v194, v96, v100
	v_cvt_pk_fp8_f32 v194, v104, v108 op_sel:[0,0,1]
	v_cvt_pk_fp8_f32 v195, v112, v116
	v_cvt_pk_fp8_f32 v195, v120, v124 op_sel:[0,0,1]
	global_store_dwordx4 v209, v[192:195], s[24:25] sc1
	v_cvt_pk_fp8_f32 v196, v65, v69
	v_cvt_pk_fp8_f32 v196, v73, v77 op_sel:[0,0,1]
	v_cvt_pk_fp8_f32 v197, v81, v85
	v_cvt_pk_fp8_f32 v197, v89, v93 op_sel:[0,0,1]
	v_cvt_pk_fp8_f32 v198, v97, v101
	v_cvt_pk_fp8_f32 v198, v105, v109 op_sel:[0,0,1]
	v_cvt_pk_fp8_f32 v199, v113, v117
	v_cvt_pk_fp8_f32 v199, v121, v125 op_sel:[0,0,1]
	global_store_dwordx4 v209, v[196:199], s[24:25] offset:2048 sc1
	v_cvt_pk_fp8_f32 v200, v66, v70
	v_cvt_pk_fp8_f32 v200, v74, v78 op_sel:[0,0,1]
	v_cvt_pk_fp8_f32 v201, v82, v86
	v_cvt_pk_fp8_f32 v201, v90, v94 op_sel:[0,0,1]
	v_cvt_pk_fp8_f32 v202, v98, v102
	v_cvt_pk_fp8_f32 v202, v106, v110 op_sel:[0,0,1]
	v_cvt_pk_fp8_f32 v203, v114, v118
	v_cvt_pk_fp8_f32 v203, v122, v126 op_sel:[0,0,1]
	global_store_dwordx4 v209, v[200:203], s[26:27] sc1
	v_cvt_pk_fp8_f32 v204, v67, v71
	v_cvt_pk_fp8_f32 v204, v75, v79 op_sel:[0,0,1]
	v_cvt_pk_fp8_f32 v205, v83, v87
	v_cvt_pk_fp8_f32 v205, v91, v95 op_sel:[0,0,1]
	v_cvt_pk_fp8_f32 v206, v99, v103
	v_cvt_pk_fp8_f32 v206, v107, v111 op_sel:[0,0,1]
	v_cvt_pk_fp8_f32 v207, v115, v119
	v_cvt_pk_fp8_f32 v207, v123, v127 op_sel:[0,0,1]
	global_store_dwordx4 v209, v[204:207], s[26:27] offset:2048 sc1
	s_waitcnt vmcnt(24)
	s_add_i32 s1, s21, 14
	s_and_b32 s1, s1, 15
	s_lshl_b32 s1, s1, 2
	s_add_i32 s1, s1, s20
	s_lshr_b32 s2, s1, 10
	s_and_b32 s4, s1, 0x3ff
	s_lshr_b32 s5, s4, 6
	s_and_b32 s4, s4, 63
	s_lshl_b32 s12, s2, 22
	s_lshl_b32 s13, s4, 16
	s_add_i32 s12, s12, s13
	s_lshl_b32 s13, s5, 7
	s_add_i32 s12, s12, s13
	s_add_u32 s24, s90, s12
	s_addc_u32 s25, s91, 0
	s_add_u32 s24, s24, 0x3b100000
	s_addc_u32 s25, s25, 0
	s_add_u32 s26, s24, 0x1000
	s_addc_u32 s27, s25, 0
	v_pk_mul_f32 v[128:129], v[128:129], s[16:17] op_sel_hi:[1,0]
	v_pk_mul_f32 v[130:131], v[130:131], s[16:17] op_sel_hi:[1,0]
	v_pk_mul_f32 v[132:133], v[132:133], s[16:17] op_sel_hi:[1,0]
	v_pk_mul_f32 v[134:135], v[134:135], s[16:17] op_sel_hi:[1,0]
	v_pk_mul_f32 v[136:137], v[136:137], s[16:17] op_sel_hi:[1,0]
	v_pk_mul_f32 v[138:139], v[138:139], s[16:17] op_sel_hi:[1,0]
	v_pk_mul_f32 v[140:141], v[140:141], s[16:17] op_sel_hi:[1,0]
	v_pk_mul_f32 v[142:143], v[142:143], s[16:17] op_sel_hi:[1,0]
	v_pk_mul_f32 v[144:145], v[144:145], s[16:17] op_sel_hi:[1,0]
	v_pk_mul_f32 v[146:147], v[146:147], s[16:17] op_sel_hi:[1,0]
	v_pk_mul_f32 v[148:149], v[148:149], s[16:17] op_sel_hi:[1,0]
	v_pk_mul_f32 v[150:151], v[150:151], s[16:17] op_sel_hi:[1,0]
	v_pk_mul_f32 v[152:153], v[152:153], s[16:17] op_sel_hi:[1,0]
	v_pk_mul_f32 v[154:155], v[154:155], s[16:17] op_sel_hi:[1,0]
	v_pk_mul_f32 v[156:157], v[156:157], s[16:17] op_sel_hi:[1,0]
	v_pk_mul_f32 v[158:159], v[158:159], s[16:17] op_sel_hi:[1,0]
	v_pk_mul_f32 v[160:161], v[160:161], s[16:17] op_sel_hi:[1,0]
	v_pk_mul_f32 v[162:163], v[162:163], s[16:17] op_sel_hi:[1,0]
	v_pk_mul_f32 v[164:165], v[164:165], s[16:17] op_sel_hi:[1,0]
	v_pk_mul_f32 v[166:167], v[166:167], s[16:17] op_sel_hi:[1,0]
	v_pk_mul_f32 v[168:169], v[168:169], s[16:17] op_sel_hi:[1,0]
	v_pk_mul_f32 v[170:171], v[170:171], s[16:17] op_sel_hi:[1,0]
	v_pk_mul_f32 v[172:173], v[172:173], s[16:17] op_sel_hi:[1,0]
	v_pk_mul_f32 v[174:175], v[174:175], s[16:17] op_sel_hi:[1,0]
	v_pk_mul_f32 v[176:177], v[176:177], s[16:17] op_sel_hi:[1,0]
	v_pk_mul_f32 v[178:179], v[178:179], s[16:17] op_sel_hi:[1,0]
	v_pk_mul_f32 v[180:181], v[180:181], s[16:17] op_sel_hi:[1,0]
	v_pk_mul_f32 v[182:183], v[182:183], s[16:17] op_sel_hi:[1,0]
	v_pk_mul_f32 v[184:185], v[184:185], s[16:17] op_sel_hi:[1,0]
	v_pk_mul_f32 v[186:187], v[186:187], s[16:17] op_sel_hi:[1,0]
	v_pk_mul_f32 v[188:189], v[188:189], s[16:17] op_sel_hi:[1,0]
	v_pk_mul_f32 v[190:191], v[190:191], s[16:17] op_sel_hi:[1,0]
	v_cvt_pk_fp8_f32 v192, v128, v132
	v_cvt_pk_fp8_f32 v192, v136, v140 op_sel:[0,0,1]
	v_cvt_pk_fp8_f32 v193, v144, v148
	v_cvt_pk_fp8_f32 v193, v152, v156 op_sel:[0,0,1]
	v_cvt_pk_fp8_f32 v194, v160, v164
	v_cvt_pk_fp8_f32 v194, v168, v172 op_sel:[0,0,1]
	v_cvt_pk_fp8_f32 v195, v176, v180
	v_cvt_pk_fp8_f32 v195, v184, v188 op_sel:[0,0,1]
	global_store_dwordx4 v209, v[192:195], s[24:25] sc1
	v_cvt_pk_fp8_f32 v196, v129, v133
	v_cvt_pk_fp8_f32 v196, v137, v141 op_sel:[0,0,1]
	v_cvt_pk_fp8_f32 v197, v145, v149
	v_cvt_pk_fp8_f32 v197, v153, v157 op_sel:[0,0,1]
	v_cvt_pk_fp8_f32 v198, v161, v165
	v_cvt_pk_fp8_f32 v198, v169, v173 op_sel:[0,0,1]
	v_cvt_pk_fp8_f32 v199, v177, v181
	v_cvt_pk_fp8_f32 v199, v185, v189 op_sel:[0,0,1]
	global_store_dwordx4 v209, v[196:199], s[24:25] offset:2048 sc1
	v_cvt_pk_fp8_f32 v200, v130, v134
	v_cvt_pk_fp8_f32 v200, v138, v142 op_sel:[0,0,1]
	v_cvt_pk_fp8_f32 v201, v146, v150
	v_cvt_pk_fp8_f32 v201, v154, v158 op_sel:[0,0,1]
	v_cvt_pk_fp8_f32 v202, v162, v166
	v_cvt_pk_fp8_f32 v202, v170, v174 op_sel:[0,0,1]
	v_cvt_pk_fp8_f32 v203, v178, v182
	v_cvt_pk_fp8_f32 v203, v186, v190 op_sel:[0,0,1]
	global_store_dwordx4 v209, v[200:203], s[26:27] sc1
	v_cvt_pk_fp8_f32 v204, v131, v135
	v_cvt_pk_fp8_f32 v204, v139, v143 op_sel:[0,0,1]
	v_cvt_pk_fp8_f32 v205, v147, v151
	v_cvt_pk_fp8_f32 v205, v155, v159 op_sel:[0,0,1]
	v_cvt_pk_fp8_f32 v206, v163, v167
	v_cvt_pk_fp8_f32 v206, v171, v175 op_sel:[0,0,1]
	v_cvt_pk_fp8_f32 v207, v179, v183
	v_cvt_pk_fp8_f32 v207, v187, v191 op_sel:[0,0,1]
	global_store_dwordx4 v209, v[204:207], s[26:27] offset:2048 sc1
	s_waitcnt vmcnt(8)
	s_add_i32 s1, s21, 15
	s_and_b32 s1, s1, 15
	s_lshl_b32 s1, s1, 2
	s_add_i32 s1, s1, s20
	s_lshr_b32 s2, s1, 10
	s_and_b32 s4, s1, 0x3ff
	s_lshr_b32 s5, s4, 6
	s_and_b32 s4, s4, 63
	s_lshl_b32 s12, s2, 22
	s_lshl_b32 s13, s4, 16
	s_add_i32 s12, s12, s13
	s_lshl_b32 s13, s5, 7
	s_add_i32 s12, s12, s13
	s_add_u32 s24, s90, s12
	s_addc_u32 s25, s91, 0
	s_add_u32 s24, s24, 0x3b100000
	s_addc_u32 s25, s25, 0
	s_add_u32 s26, s24, 0x1000
	s_addc_u32 s27, s25, 0
	v_pk_mul_f32 v[0:1], v[0:1], s[16:17] op_sel_hi:[1,0]
	v_pk_mul_f32 v[2:3], v[2:3], s[16:17] op_sel_hi:[1,0]
	v_pk_mul_f32 v[4:5], v[4:5], s[16:17] op_sel_hi:[1,0]
	v_pk_mul_f32 v[6:7], v[6:7], s[16:17] op_sel_hi:[1,0]
	v_pk_mul_f32 v[8:9], v[8:9], s[16:17] op_sel_hi:[1,0]
	v_pk_mul_f32 v[10:11], v[10:11], s[16:17] op_sel_hi:[1,0]
	v_pk_mul_f32 v[12:13], v[12:13], s[16:17] op_sel_hi:[1,0]
	v_pk_mul_f32 v[14:15], v[14:15], s[16:17] op_sel_hi:[1,0]
	v_pk_mul_f32 v[16:17], v[16:17], s[16:17] op_sel_hi:[1,0]
	v_pk_mul_f32 v[18:19], v[18:19], s[16:17] op_sel_hi:[1,0]
	v_pk_mul_f32 v[20:21], v[20:21], s[16:17] op_sel_hi:[1,0]
	v_pk_mul_f32 v[22:23], v[22:23], s[16:17] op_sel_hi:[1,0]
	v_pk_mul_f32 v[24:25], v[24:25], s[16:17] op_sel_hi:[1,0]
	v_pk_mul_f32 v[26:27], v[26:27], s[16:17] op_sel_hi:[1,0]
	v_pk_mul_f32 v[28:29], v[28:29], s[16:17] op_sel_hi:[1,0]
	v_pk_mul_f32 v[30:31], v[30:31], s[16:17] op_sel_hi:[1,0]
	v_pk_mul_f32 v[32:33], v[32:33], s[16:17] op_sel_hi:[1,0]
	v_pk_mul_f32 v[34:35], v[34:35], s[16:17] op_sel_hi:[1,0]
	v_pk_mul_f32 v[36:37], v[36:37], s[16:17] op_sel_hi:[1,0]
	v_pk_mul_f32 v[38:39], v[38:39], s[16:17] op_sel_hi:[1,0]
	v_pk_mul_f32 v[40:41], v[40:41], s[16:17] op_sel_hi:[1,0]
	v_pk_mul_f32 v[42:43], v[42:43], s[16:17] op_sel_hi:[1,0]
	v_pk_mul_f32 v[44:45], v[44:45], s[16:17] op_sel_hi:[1,0]
	v_pk_mul_f32 v[46:47], v[46:47], s[16:17] op_sel_hi:[1,0]
	v_pk_mul_f32 v[48:49], v[48:49], s[16:17] op_sel_hi:[1,0]
	v_pk_mul_f32 v[50:51], v[50:51], s[16:17] op_sel_hi:[1,0]
	v_pk_mul_f32 v[52:53], v[52:53], s[16:17] op_sel_hi:[1,0]
	v_pk_mul_f32 v[54:55], v[54:55], s[16:17] op_sel_hi:[1,0]
	v_pk_mul_f32 v[56:57], v[56:57], s[16:17] op_sel_hi:[1,0]
	v_pk_mul_f32 v[58:59], v[58:59], s[16:17] op_sel_hi:[1,0]
	v_pk_mul_f32 v[60:61], v[60:61], s[16:17] op_sel_hi:[1,0]
	v_pk_mul_f32 v[62:63], v[62:63], s[16:17] op_sel_hi:[1,0]
	v_cvt_pk_fp8_f32 v192, v0, v4
	v_cvt_pk_fp8_f32 v192, v8, v12 op_sel:[0,0,1]
	v_cvt_pk_fp8_f32 v193, v16, v20
	v_cvt_pk_fp8_f32 v193, v24, v28 op_sel:[0,0,1]
	v_cvt_pk_fp8_f32 v194, v32, v36
	v_cvt_pk_fp8_f32 v194, v40, v44 op_sel:[0,0,1]
	v_cvt_pk_fp8_f32 v195, v48, v52
	v_cvt_pk_fp8_f32 v195, v56, v60 op_sel:[0,0,1]
	global_store_dwordx4 v209, v[192:195], s[24:25] sc1
	v_cvt_pk_fp8_f32 v196, v1, v5
	v_cvt_pk_fp8_f32 v196, v9, v13 op_sel:[0,0,1]
	v_cvt_pk_fp8_f32 v197, v17, v21
	v_cvt_pk_fp8_f32 v197, v25, v29 op_sel:[0,0,1]
	v_cvt_pk_fp8_f32 v198, v33, v37
	v_cvt_pk_fp8_f32 v198, v41, v45 op_sel:[0,0,1]
	v_cvt_pk_fp8_f32 v199, v49, v53
	v_cvt_pk_fp8_f32 v199, v57, v61 op_sel:[0,0,1]
	global_store_dwordx4 v209, v[196:199], s[24:25] offset:2048 sc1
	v_cvt_pk_fp8_f32 v200, v2, v6
	v_cvt_pk_fp8_f32 v200, v10, v14 op_sel:[0,0,1]
	v_cvt_pk_fp8_f32 v201, v18, v22
	v_cvt_pk_fp8_f32 v201, v26, v30 op_sel:[0,0,1]
	v_cvt_pk_fp8_f32 v202, v34, v38
	v_cvt_pk_fp8_f32 v202, v42, v46 op_sel:[0,0,1]
	v_cvt_pk_fp8_f32 v203, v50, v54
	v_cvt_pk_fp8_f32 v203, v58, v62 op_sel:[0,0,1]
	global_store_dwordx4 v209, v[200:203], s[26:27] sc1
	v_cvt_pk_fp8_f32 v204, v3, v7
	v_cvt_pk_fp8_f32 v204, v11, v15 op_sel:[0,0,1]
	v_cvt_pk_fp8_f32 v205, v19, v23
	v_cvt_pk_fp8_f32 v205, v27, v31 op_sel:[0,0,1]
	v_cvt_pk_fp8_f32 v206, v35, v39
	v_cvt_pk_fp8_f32 v206, v43, v47 op_sel:[0,0,1]
	v_cvt_pk_fp8_f32 v207, v51, v55
	v_cvt_pk_fp8_f32 v207, v59, v63 op_sel:[0,0,1]
	global_store_dwordx4 v209, v[204:207], s[26:27] offset:2048 sc1
	s_waitcnt vmcnt(0)
	v_readlane_b32 s3, v255, 4
